# gate/router dot products in the row phases re-expressed with packed f32 FMAs (v_pk_mul_f32/v_pk_fma_f32 pair accumulator + one add): 384 scalar VALU ops per row become 136; f32 throughout, summation o
# speedup vs baseline: 1.0226x; 1.0017x over previous
; #define LAS __attribute__((address_space(3)))
; __device__ __forceinline__ unsigned cvtpk(float lo, float hi) { f32x2 v = {lo, hi}; bf16x2_t b = __builtin_convertvector(v, bf16x2_t); return __builtin_bit_cast(unsigned, b); }
; __device__ __forceinline__ float wave_max(float v) { return lane63(scan64<true>(v)); }
; template <int YMODE, int EXTRA, bool NORM_OUT, bool XN8  , bool XIN_BF = false  , bool XOUT_BF = false  > ...
;     ...
;                 if (XN8) {
;                     float am = 0.f;
; #pragma unroll
;                     for (int j = 0; j < 8; ++j) am = fmaxf(fmaxf(am, fmaxf(fabsf(x[j][0]), fabsf(x[j][1]))), fmaxf(fabsf(x[j][2]), fabsf(x[j][3])));
;                     am = wave_max(am);
;                     const float inv = am > 0.f ? 127.f / am : 0.f;
;                     if (F.lane == 0) { rowmax[row] = am; if (EXTRA == 2) route[384 + rl] = am; }
; #pragma unroll
;                     for (int j = 0; j < 8; ++j) *(unsigned*)((unsigned char*)XN + row * D + 256 * j + 4 * F.lane) = pack_i8x4(x[j][0] * inv, x[j][1] * inv, x[j][2] * inv, x[j][3] * inv);
;                 } else {
; #pragma unroll
;                     for (int j = 0; j < 8; ++j) { u32x2 w; w.x = cvtpk(x[j][0], x[j][1]); w.y = cvtpk(x[j][2], x[j][3]); *(u32x2*)(XN + row * D + 256 * j + 4 * F.lane) = w; }
;                 }
;                 if (EXTRA) {
;                     float d8[8];
; #pragma unroll
;                     for (int e = 0; e < 8; ++e) { float s = 0.f;
; #pragma unroll
;                         for (int j = 0; j < 8; ++j) { const f32x4 w = *(const LAS f32x4*)(we + e * D + 256 * j + 4 * F.lane); s += (x[j][0] * w[0] + x[j][1] * w[1]) + (x[j][2] * w[2] + x[j][3] * w[3]); }
.LBB0_112:
	s_or_b64 exec, exec, s[36:37]
	ds_read_b128 v[196:199], v88
	ds_read_b128 v[200:203], v88 offset:1024
	ds_read_b128 v[204:207], v88 offset:2048
	ds_read_b128 v[208:211], v88 offset:3072
	ds_read_b128 v[212:215], v88 offset:4096
	ds_read_b128 v[216:219], v88 offset:5120
	ds_read_b128 v[220:223], v88 offset:6144
	ds_read_b128 v[224:227], v88 offset:7168
	ds_read_b128 v[228:231], v88 offset:8192
	ds_read_b128 v[232:235], v88 offset:9216
	ds_read_b128 v[240:243], v88 offset:10240
	ds_read_b128 v[244:247], v88 offset:11264
	v_div_scale_f32 v1, s[36:37], s34, s34, v93
	v_rcp_f32_e32 v83, v1
	v_mov_b32_e32 v95, s34
	v_div_scale_f32 v95, vcc, s40, v95, s40
	v_fma_f32 v96, -v1, v83, 1.0
	v_fmac_f32_e32 v83, v96, v83
	v_mul_f32_e32 v96, v95, v83
	v_fma_f32 v97, -v1, v96, v95
	v_fmac_f32_e32 v96, v97, v83
	v_fma_f32 v1, -v1, v96, v95
	v_div_fmas_f32 v1, v1, v83, v96
	v_div_fixup_f32 v1, v1, s34, v93
	v_cmp_gt_f32_e64 vcc, s34, 0
	s_lshl_b64 s[36:37], s[26:27], 11
	v_lshl_add_u64 v[100:101], v[80:81], 0, s[36:37]
	v_cndmask_b32_e32 v1, 0, v1, vcc
	v_mul_f32_e32 v95, v65, v1
	v_mul_f32_e32 v83, v64, v1
	v_mul_f32_e32 v96, v62, v1
	v_mul_f32_e32 v97, v63, v1
	v_med3_f32 v95, v95, s41, v93
	v_med3_f32 v83, v83, s41, v93
	v_rndne_f32_e32 v95, v95
	v_med3_f32 v96, v96, s41, v93
	v_med3_f32 v97, v97, s41, v93
	v_rndne_f32_e32 v83, v83
	v_cvt_i32_f32_e32 v95, v95
	v_rndne_f32_e32 v96, v96
	v_rndne_f32_e32 v97, v97
	v_cvt_i32_f32_e32 v83, v83
	v_cvt_i32_f32_sdwa v96, v96 dst_sel:WORD_1 dst_unused:UNUSED_PAD src0_sel:DWORD
	v_cvt_i32_f32_e32 v97, v97
	v_lshlrev_b32_e32 v95, 8, v95
	v_and_b32_e32 v95, 0xff00, v95
	v_and_b32_e32 v96, 0xff0000, v96
	v_perm_b32 v83, v97, v83, s42
	v_or3_b32 v83, v83, v95, v96
	v_mul_f32_e32 v95, v61, v1
	global_store_dword v[100:101], v83, off
	v_mul_f32_e32 v83, v60, v1
	v_mul_f32_e32 v96, v58, v1
	v_mul_f32_e32 v97, v59, v1
	v_med3_f32 v95, v95, s41, v93
	v_med3_f32 v83, v83, s41, v93
	v_rndne_f32_e32 v95, v95
	v_med3_f32 v96, v96, s41, v93
	v_med3_f32 v97, v97, s41, v93
	v_rndne_f32_e32 v83, v83
	v_cvt_i32_f32_e32 v95, v95
	v_rndne_f32_e32 v96, v96
	v_rndne_f32_e32 v97, v97
	v_cvt_i32_f32_e32 v83, v83
	v_cvt_i32_f32_sdwa v96, v96 dst_sel:WORD_1 dst_unused:UNUSED_PAD src0_sel:DWORD
	v_cvt_i32_f32_e32 v97, v97
	v_lshlrev_b32_e32 v95, 8, v95
	v_and_b32_e32 v95, 0xff00, v95
	v_and_b32_e32 v96, 0xff0000, v96
	v_perm_b32 v83, v97, v83, s42
	v_or3_b32 v83, v83, v95, v96
	v_mul_f32_e32 v95, v57, v1
	global_store_dword v[100:101], v83, off offset:256
	v_mul_f32_e32 v83, v56, v1
	v_mul_f32_e32 v96, v54, v1
	v_mul_f32_e32 v97, v55, v1
	v_med3_f32 v95, v95, s41, v93
	v_med3_f32 v83, v83, s41, v93
	v_rndne_f32_e32 v95, v95
	v_med3_f32 v96, v96, s41, v93
	v_med3_f32 v97, v97, s41, v93
	v_rndne_f32_e32 v83, v83
	v_cvt_i32_f32_e32 v95, v95
	v_rndne_f32_e32 v96, v96
	v_rndne_f32_e32 v97, v97
	v_cvt_i32_f32_e32 v83, v83
	v_cvt_i32_f32_sdwa v96, v96 dst_sel:WORD_1 dst_unused:UNUSED_PAD src0_sel:DWORD
	v_cvt_i32_f32_e32 v97, v97
	v_lshlrev_b32_e32 v95, 8, v95
	v_and_b32_e32 v95, 0xff00, v95
	v_and_b32_e32 v96, 0xff0000, v96
	v_perm_b32 v83, v97, v83, s42
	v_or3_b32 v83, v83, v95, v96
	v_mul_f32_e32 v95, v53, v1
	global_store_dword v[100:101], v83, off offset:512
	v_mul_f32_e32 v83, v52, v1
	v_mul_f32_e32 v96, v50, v1
	v_mul_f32_e32 v97, v51, v1
	v_med3_f32 v95, v95, s41, v93
	v_med3_f32 v83, v83, s41, v93
	v_rndne_f32_e32 v95, v95
	v_med3_f32 v96, v96, s41, v93
	v_med3_f32 v97, v97, s41, v93
	v_rndne_f32_e32 v83, v83
	v_cvt_i32_f32_e32 v95, v95
	v_rndne_f32_e32 v96, v96
	v_rndne_f32_e32 v97, v97
	v_cvt_i32_f32_e32 v83, v83
	v_cvt_i32_f32_sdwa v96, v96 dst_sel:WORD_1 dst_unused:UNUSED_PAD src0_sel:DWORD
	v_cvt_i32_f32_e32 v97, v97
	v_lshlrev_b32_e32 v95, 8, v95
	v_and_b32_e32 v95, 0xff00, v95
	v_and_b32_e32 v96, 0xff0000, v96
	v_perm_b32 v83, v97, v83, s42
	v_or3_b32 v83, v83, v95, v96
	v_mul_f32_e32 v95, v49, v1
	global_store_dword v[100:101], v83, off offset:768
	v_mul_f32_e32 v83, v48, v1
	v_mul_f32_e32 v96, v46, v1
	v_mul_f32_e32 v97, v47, v1
	v_med3_f32 v95, v95, s41, v93
	v_med3_f32 v83, v83, s41, v93
	v_rndne_f32_e32 v95, v95
	v_med3_f32 v96, v96, s41, v93
	v_med3_f32 v97, v97, s41, v93
	v_rndne_f32_e32 v83, v83
	v_cvt_i32_f32_e32 v95, v95
	v_rndne_f32_e32 v96, v96
	v_rndne_f32_e32 v97, v97
	v_cvt_i32_f32_e32 v83, v83
	v_cvt_i32_f32_sdwa v96, v96 dst_sel:WORD_1 dst_unused:UNUSED_PAD src0_sel:DWORD
	v_cvt_i32_f32_e32 v97, v97
	v_lshlrev_b32_e32 v95, 8, v95
	v_and_b32_e32 v95, 0xff00, v95
	v_and_b32_e32 v96, 0xff0000, v96
	v_perm_b32 v83, v97, v83, s42
	v_or3_b32 v83, v83, v95, v96
	v_mul_f32_e32 v95, v45, v1
	global_store_dword v[100:101], v83, off offset:1024
	v_mul_f32_e32 v83, v44, v1
	v_mul_f32_e32 v96, v42, v1
	v_mul_f32_e32 v97, v43, v1
	v_med3_f32 v95, v95, s41, v93
	v_med3_f32 v83, v83, s41, v93
	v_rndne_f32_e32 v95, v95
	v_med3_f32 v96, v96, s41, v93
	v_med3_f32 v97, v97, s41, v93
	v_rndne_f32_e32 v83, v83
	v_cvt_i32_f32_e32 v95, v95
	v_rndne_f32_e32 v96, v96
	v_rndne_f32_e32 v97, v97
	v_cvt_i32_f32_e32 v83, v83
	v_cvt_i32_f32_sdwa v96, v96 dst_sel:WORD_1 dst_unused:UNUSED_PAD src0_sel:DWORD
	v_cvt_i32_f32_e32 v97, v97
	v_lshlrev_b32_e32 v95, 8, v95
	v_and_b32_e32 v95, 0xff00, v95
	v_and_b32_e32 v96, 0xff0000, v96
	v_perm_b32 v83, v97, v83, s42
	v_or3_b32 v83, v83, v95, v96
	v_mul_f32_e32 v95, v41, v1
	global_store_dword v[100:101], v83, off offset:1280
	v_mul_f32_e32 v83, v40, v1
	v_mul_f32_e32 v96, v38, v1
	v_mul_f32_e32 v97, v39, v1
	v_med3_f32 v95, v95, s41, v93
	v_med3_f32 v83, v83, s41, v93
	v_rndne_f32_e32 v95, v95
	v_med3_f32 v96, v96, s41, v93
	v_med3_f32 v97, v97, s41, v93
	v_rndne_f32_e32 v83, v83
	v_cvt_i32_f32_e32 v95, v95
	v_rndne_f32_e32 v96, v96
	v_rndne_f32_e32 v97, v97
	v_cvt_i32_f32_e32 v83, v83
	v_cvt_i32_f32_sdwa v96, v96 dst_sel:WORD_1 dst_unused:UNUSED_PAD src0_sel:DWORD
	v_cvt_i32_f32_e32 v97, v97
	v_lshlrev_b32_e32 v95, 8, v95
	v_and_b32_e32 v95, 0xff00, v95
	v_and_b32_e32 v96, 0xff0000, v96
	v_perm_b32 v83, v97, v83, s42
	v_or3_b32 v83, v83, v95, v96
	v_mul_f32_e32 v95, v37, v1
	v_mul_f32_e32 v96, v34, v1
	global_store_dword v[100:101], v83, off offset:1536
	v_mul_f32_e32 v83, v36, v1
	v_mul_f32_e32 v1, v35, v1
	v_med3_f32 v95, v95, s41, v93
	v_med3_f32 v96, v96, s41, v93
	v_med3_f32 v83, v83, s41, v93
	v_rndne_f32_e32 v95, v95
	v_rndne_f32_e32 v96, v96
	v_med3_f32 v1, v1, s41, v93
	v_rndne_f32_e32 v83, v83
	v_cvt_i32_f32_e32 v95, v95
	v_cvt_i32_f32_sdwa v96, v96 dst_sel:WORD_1 dst_unused:UNUSED_PAD src0_sel:DWORD
	v_rndne_f32_e32 v1, v1
	v_cvt_i32_f32_e32 v83, v83
	v_cvt_i32_f32_e32 v1, v1
	v_lshlrev_b32_e32 v95, 8, v95
	v_and_b32_e32 v102, 0xff0000, v96
	s_nop 0
	v_and_b32_e32 v95, 0xff00, v95
	v_perm_b32 v1, v1, v83, s42
	v_or3_b32 v1, v1, v95, v102
	global_store_dword v[100:101], v1, off offset:1792
	s_nop 0
	s_waitcnt lgkmcnt(12)
; #define LAS __attribute__((address_space(3)))
; __device__ __forceinline__ float wave_sum(float v) { return lane63(scan64<false>(v)); }
; template <int YMODE, int EXTRA, bool NORM_OUT, bool XN8  , bool XIN_BF = false  , bool XOUT_BF = false  > ...
;     ...
;                     for (int e = 0; e < 8; ++e) { float s = 0.f;
; #pragma unroll
;                         for (int j = 0; j < 8; ++j) { const f32x4 w = *(const LAS f32x4*)(we + e * D + 256 * j + 4 * F.lane); s += (x[j][0] * w[0] + x[j][1] * w[1]) + (x[j][2] * w[2] + x[j][3] * w[3]); }
;                         d8[e] = wave_sum(s); asm volatile("" ::: "memory"); }
	s_waitcnt lgkmcnt(11)
	v_pk_mul_f32 v[190:191], v[64:65], v[196:197]
	ds_read_b128 v[248:251], v88 offset:12288
	v_pk_fma_f32 v[190:191], v[62:63], v[198:199], v[190:191]
	s_waitcnt lgkmcnt(11)
	v_pk_fma_f32 v[190:191], v[60:61], v[200:201], v[190:191]
	ds_read_b128 v[196:199], v88 offset:13312
	v_pk_fma_f32 v[190:191], v[58:59], v[202:203], v[190:191]
	s_waitcnt lgkmcnt(11)
	v_pk_fma_f32 v[190:191], v[56:57], v[204:205], v[190:191]
	ds_read_b128 v[200:203], v88 offset:14336
	v_pk_fma_f32 v[190:191], v[54:55], v[206:207], v[190:191]
	s_waitcnt lgkmcnt(11)
	v_pk_fma_f32 v[190:191], v[52:53], v[208:209], v[190:191]
	ds_read_b128 v[204:207], v88 offset:15360
	v_pk_fma_f32 v[190:191], v[50:51], v[210:211], v[190:191]
	s_waitcnt lgkmcnt(11)
	v_pk_fma_f32 v[190:191], v[48:49], v[212:213], v[190:191]
	ds_read_b128 v[208:211], v88 offset:16384
	v_pk_fma_f32 v[190:191], v[46:47], v[214:215], v[190:191]
	s_waitcnt lgkmcnt(11)
	v_pk_fma_f32 v[190:191], v[44:45], v[216:217], v[190:191]
	ds_read_b128 v[212:215], v88 offset:17408
	v_pk_fma_f32 v[190:191], v[42:43], v[218:219], v[190:191]
	s_waitcnt lgkmcnt(11)
	v_pk_fma_f32 v[190:191], v[40:41], v[220:221], v[190:191]
	ds_read_b128 v[216:219], v88 offset:18432
	v_pk_fma_f32 v[190:191], v[38:39], v[222:223], v[190:191]
	s_waitcnt lgkmcnt(11)
	v_pk_fma_f32 v[190:191], v[36:37], v[224:225], v[190:191]
	ds_read_b128 v[220:223], v88 offset:19456
	v_pk_fma_f32 v[190:191], v[34:35], v[226:227], v[190:191]
	v_add_f32_e32 v1, v190, v191
	v_mov_b32_e32 v83, 0
	s_nop 0
	s_nop 0
	v_add_f32_dpp v1, v1, v1 row_shr:1 row_mask:0xf bank_mask:0xf bound_ctrl:1
	s_nop 0
	s_waitcnt lgkmcnt(10)
	v_pk_mul_f32 v[192:193], v[60:61], v[232:233]
	ds_read_b128 v[224:227], v88 offset:20480
	v_pk_fma_f32 v[192:193], v[58:59], v[234:235], v[192:193]
	v_add_f32_dpp v1, v1, v1 row_shr:2 row_mask:0xf bank_mask:0xf bound_ctrl:1
	s_nop 0
	s_nop 0
	v_add_f32_dpp v1, v1, v1 row_shr:4 row_mask:0xf bank_mask:0xf bound_ctrl:1
	s_nop 1
	v_add_f32_dpp v1, v1, v1 row_shr:8 row_mask:0xf bank_mask:0xf bound_ctrl:1
	s_nop 1
	v_mov_b32_dpp v83, v1 row_bcast:15 row_mask:0xa bank_mask:0xf
	v_add_f32_e32 v1, v1, v83
	v_mov_b32_e32 v83, 0
	s_nop 1
	v_mov_b32_dpp v83, v1 row_bcast:31 row_mask:0xc bank_mask:0xf
	v_add_f32_e32 v1, v1, v83
	v_pk_fma_f32 v[192:193], v[64:65], v[228:229], v[192:193]
	ds_read_b128 v[232:235], v88 offset:21504
	v_pk_fma_f32 v[192:193], v[62:63], v[230:231], v[192:193]
	v_readlane_b32 s34, v1, 63
	s_nop 0
	s_nop 0
	s_nop 0
	s_waitcnt lgkmcnt(11)
	v_pk_fma_f32 v[192:193], v[56:57], v[240:241], v[192:193]
	ds_read_b128 v[228:231], v88 offset:22528
	v_pk_fma_f32 v[192:193], v[54:55], v[242:243], v[192:193]
	s_waitcnt lgkmcnt(11)
	v_pk_fma_f32 v[192:193], v[52:53], v[244:245], v[192:193]
	ds_read_b128 v[240:243], v88 offset:23552
	v_pk_fma_f32 v[192:193], v[50:51], v[246:247], v[192:193]
	s_waitcnt lgkmcnt(11)
	v_pk_fma_f32 v[192:193], v[48:49], v[248:249], v[192:193]
	ds_read_b128 v[244:247], v88 offset:24576
	v_pk_fma_f32 v[192:193], v[46:47], v[250:251], v[192:193]
	s_waitcnt lgkmcnt(11)
	v_pk_fma_f32 v[192:193], v[44:45], v[196:197], v[192:193]
	ds_read_b128 v[248:251], v88 offset:25600
	v_pk_fma_f32 v[192:193], v[42:43], v[198:199], v[192:193]
	s_waitcnt lgkmcnt(11)
	v_pk_fma_f32 v[192:193], v[40:41], v[200:201], v[192:193]
	ds_read_b128 v[196:199], v88 offset:26624
	v_pk_fma_f32 v[192:193], v[38:39], v[202:203], v[192:193]
	s_waitcnt lgkmcnt(11)
	v_pk_fma_f32 v[192:193], v[36:37], v[204:205], v[192:193]
	ds_read_b128 v[200:203], v88 offset:27648
	v_pk_fma_f32 v[192:193], v[34:35], v[206:207], v[192:193]
	v_add_f32_e32 v1, v192, v193
	v_mov_b32_e32 v83, 0
	s_nop 0
	s_nop 0
	v_add_f32_dpp v1, v1, v1 row_shr:1 row_mask:0xf bank_mask:0xf bound_ctrl:1
	s_nop 0
	s_waitcnt lgkmcnt(10)
	v_pk_mul_f32 v[190:191], v[60:61], v[212:213]
	ds_read_b128 v[204:207], v88 offset:28672
	v_pk_fma_f32 v[190:191], v[58:59], v[214:215], v[190:191]
	v_add_f32_dpp v1, v1, v1 row_shr:2 row_mask:0xf bank_mask:0xf bound_ctrl:1
	s_nop 0
	s_nop 0
	v_add_f32_dpp v1, v1, v1 row_shr:4 row_mask:0xf bank_mask:0xf bound_ctrl:1
	s_nop 1
	v_add_f32_dpp v1, v1, v1 row_shr:8 row_mask:0xf bank_mask:0xf bound_ctrl:1
	s_nop 1
	v_mov_b32_dpp v83, v1 row_bcast:15 row_mask:0xa bank_mask:0xf
	v_add_f32_e32 v1, v1, v83
	v_mov_b32_e32 v83, 0
	s_nop 1
	v_mov_b32_dpp v83, v1 row_bcast:31 row_mask:0xc bank_mask:0xf
	v_add_f32_e32 v1, v1, v83
	v_pk_fma_f32 v[190:191], v[64:65], v[208:209], v[190:191]
	ds_read_b128 v[212:215], v88 offset:29696
	v_pk_fma_f32 v[190:191], v[62:63], v[210:211], v[190:191]
	v_readlane_b32 s38, v1, 63
	s_nop 0
	s_nop 0
	s_nop 0
	s_waitcnt lgkmcnt(11)
	v_pk_fma_f32 v[190:191], v[56:57], v[216:217], v[190:191]
	ds_read_b128 v[208:211], v88 offset:30720
	v_pk_fma_f32 v[190:191], v[54:55], v[218:219], v[190:191]
	s_waitcnt lgkmcnt(11)
	v_pk_fma_f32 v[190:191], v[52:53], v[220:221], v[190:191]
	ds_read_b128 v[216:219], v88 offset:31744
	v_pk_fma_f32 v[190:191], v[50:51], v[222:223], v[190:191]
	s_waitcnt lgkmcnt(11)
	v_pk_fma_f32 v[190:191], v[48:49], v[224:225], v[190:191]
	ds_read_b128 v[220:223], v88 offset:32768
	v_pk_fma_f32 v[190:191], v[46:47], v[226:227], v[190:191]
	s_waitcnt lgkmcnt(11)
	v_pk_fma_f32 v[190:191], v[44:45], v[232:233], v[190:191]
	ds_read_b128 v[224:227], v88 offset:33792
	v_pk_fma_f32 v[190:191], v[42:43], v[234:235], v[190:191]
	s_waitcnt lgkmcnt(11)
	v_pk_fma_f32 v[190:191], v[40:41], v[228:229], v[190:191]
	ds_read_b128 v[232:235], v88 offset:34816
	v_pk_fma_f32 v[190:191], v[38:39], v[230:231], v[190:191]
	s_waitcnt lgkmcnt(11)
; #define LAS __attribute__((address_space(3)))
; __device__ __forceinline__ float wave_sum(float v) { return lane63(scan64<false>(v)); }
; template <int YMODE, int EXTRA, bool NORM_OUT, bool XN8  , bool XIN_BF = false  , bool XOUT_BF = false  > ...
;     ...
;                     for (int e = 0; e < 8; ++e) { float s = 0.f;
; #pragma unroll
;                         for (int j = 0; j < 8; ++j) { const f32x4 w = *(const LAS f32x4*)(we + e * D + 256 * j + 4 * F.lane); s += (x[j][0] * w[0] + x[j][1] * w[1]) + (x[j][2] * w[2] + x[j][3] * w[3]); }
;                         d8[e] = wave_sum(s); asm volatile("" ::: "memory"); }
	v_pk_fma_f32 v[190:191], v[36:37], v[240:241], v[190:191]
	ds_read_b128 v[228:231], v88 offset:35840
	v_pk_fma_f32 v[190:191], v[34:35], v[242:243], v[190:191]
	v_add_f32_e32 v1, v190, v191
	v_mov_b32_e32 v83, 0
	s_nop 0
	s_nop 0
	v_add_f32_dpp v1, v1, v1 row_shr:1 row_mask:0xf bank_mask:0xf bound_ctrl:1
	s_nop 0
	s_waitcnt lgkmcnt(10)
	v_pk_mul_f32 v[192:193], v[60:61], v[248:249]
	ds_read_b128 v[240:243], v88 offset:36864
	v_pk_fma_f32 v[192:193], v[58:59], v[250:251], v[192:193]
	v_add_f32_dpp v1, v1, v1 row_shr:2 row_mask:0xf bank_mask:0xf bound_ctrl:1
	s_nop 0
	s_nop 0
	v_add_f32_dpp v1, v1, v1 row_shr:4 row_mask:0xf bank_mask:0xf bound_ctrl:1
	s_nop 1
	v_add_f32_dpp v1, v1, v1 row_shr:8 row_mask:0xf bank_mask:0xf bound_ctrl:1
	s_nop 1
	v_mov_b32_dpp v83, v1 row_bcast:15 row_mask:0xa bank_mask:0xf
	v_add_f32_e32 v1, v1, v83
	v_mov_b32_e32 v83, 0
	s_nop 1
	v_mov_b32_dpp v83, v1 row_bcast:31 row_mask:0xc bank_mask:0xf
	v_add_f32_e32 v1, v1, v83
	v_pk_fma_f32 v[192:193], v[64:65], v[244:245], v[192:193]
	ds_read_b128 v[248:251], v88 offset:37888
	v_pk_fma_f32 v[192:193], v[62:63], v[246:247], v[192:193]
	v_readlane_b32 s39, v1, 63
	s_nop 0
	s_nop 0
	s_nop 0
	s_waitcnt lgkmcnt(11)
	v_pk_fma_f32 v[192:193], v[56:57], v[196:197], v[192:193]
	ds_read_b128 v[244:247], v88 offset:38912
	v_pk_fma_f32 v[192:193], v[54:55], v[198:199], v[192:193]
	s_waitcnt lgkmcnt(11)
	v_pk_fma_f32 v[192:193], v[52:53], v[200:201], v[192:193]
	ds_read_b128 v[196:199], v88 offset:39936
	v_pk_fma_f32 v[192:193], v[50:51], v[202:203], v[192:193]
	s_waitcnt lgkmcnt(11)
	v_pk_fma_f32 v[192:193], v[48:49], v[204:205], v[192:193]
	ds_read_b128 v[200:203], v88 offset:40960
	v_pk_fma_f32 v[192:193], v[46:47], v[206:207], v[192:193]
	s_waitcnt lgkmcnt(11)
	v_pk_fma_f32 v[192:193], v[44:45], v[212:213], v[192:193]
	ds_read_b128 v[204:207], v88 offset:41984
	v_pk_fma_f32 v[192:193], v[42:43], v[214:215], v[192:193]
	s_waitcnt lgkmcnt(11)
	v_pk_fma_f32 v[192:193], v[40:41], v[208:209], v[192:193]
	ds_read_b128 v[212:215], v88 offset:43008
	v_pk_fma_f32 v[192:193], v[38:39], v[210:211], v[192:193]
	s_waitcnt lgkmcnt(11)
	v_pk_fma_f32 v[192:193], v[36:37], v[216:217], v[192:193]
	ds_read_b128 v[208:211], v88 offset:44032
	v_pk_fma_f32 v[192:193], v[34:35], v[218:219], v[192:193]
	v_add_f32_e32 v1, v192, v193
	v_mov_b32_e32 v83, 0
	s_nop 0
	s_nop 0
	v_add_f32_dpp v1, v1, v1 row_shr:1 row_mask:0xf bank_mask:0xf bound_ctrl:1
	s_nop 0
	s_waitcnt lgkmcnt(10)
	v_pk_mul_f32 v[190:191], v[60:61], v[224:225]
	ds_read_b128 v[216:219], v88 offset:45056
	v_pk_fma_f32 v[190:191], v[58:59], v[226:227], v[190:191]
	v_add_f32_dpp v1, v1, v1 row_shr:2 row_mask:0xf bank_mask:0xf bound_ctrl:1
	s_nop 0
	s_nop 0
	v_add_f32_dpp v1, v1, v1 row_shr:4 row_mask:0xf bank_mask:0xf bound_ctrl:1
	s_nop 1
	v_add_f32_dpp v1, v1, v1 row_shr:8 row_mask:0xf bank_mask:0xf bound_ctrl:1
	s_nop 1
	v_mov_b32_dpp v83, v1 row_bcast:15 row_mask:0xa bank_mask:0xf
	v_add_f32_e32 v1, v1, v83
	v_mov_b32_e32 v83, 0
	s_nop 1
	v_mov_b32_dpp v83, v1 row_bcast:31 row_mask:0xc bank_mask:0xf
	v_add_f32_e32 v1, v1, v83
	v_pk_fma_f32 v[190:191], v[64:65], v[220:221], v[190:191]
	ds_read_b128 v[224:227], v88 offset:46080
	v_pk_fma_f32 v[190:191], v[62:63], v[222:223], v[190:191]
	v_readlane_b32 s60, v1, 63
	s_nop 0
	s_nop 0
	s_nop 0
	s_waitcnt lgkmcnt(11)
	v_pk_fma_f32 v[190:191], v[56:57], v[232:233], v[190:191]
	ds_read_b128 v[220:223], v88 offset:47104
	v_pk_fma_f32 v[190:191], v[54:55], v[234:235], v[190:191]
	s_waitcnt lgkmcnt(11)
	v_pk_fma_f32 v[190:191], v[52:53], v[228:229], v[190:191]
	ds_read_b128 v[232:235], v88 offset:48128
	v_pk_fma_f32 v[190:191], v[50:51], v[230:231], v[190:191]
	s_waitcnt lgkmcnt(11)
	v_pk_fma_f32 v[190:191], v[48:49], v[240:241], v[190:191]
	ds_read_b128 v[228:231], v88 offset:49152
	v_pk_fma_f32 v[190:191], v[46:47], v[242:243], v[190:191]
	s_waitcnt lgkmcnt(11)
	v_pk_fma_f32 v[190:191], v[44:45], v[248:249], v[190:191]
	ds_read_b128 v[240:243], v88 offset:50176
	v_pk_fma_f32 v[190:191], v[42:43], v[250:251], v[190:191]
	s_waitcnt lgkmcnt(11)
	v_pk_fma_f32 v[190:191], v[40:41], v[244:245], v[190:191]
	ds_read_b128 v[248:251], v88 offset:51200
	v_pk_fma_f32 v[190:191], v[38:39], v[246:247], v[190:191]
	s_waitcnt lgkmcnt(11)
	v_pk_fma_f32 v[190:191], v[36:37], v[196:197], v[190:191]
	ds_read_b128 v[244:247], v88 offset:52224
	v_pk_fma_f32 v[190:191], v[34:35], v[198:199], v[190:191]
	v_add_f32_e32 v1, v190, v191
	v_mov_b32_e32 v83, 0
	s_nop 0
	s_nop 0
	v_add_f32_dpp v1, v1, v1 row_shr:1 row_mask:0xf bank_mask:0xf bound_ctrl:1
	s_nop 0
	s_waitcnt lgkmcnt(10)
	v_pk_mul_f32 v[192:193], v[60:61], v[204:205]
	ds_read_b128 v[196:199], v88 offset:53248
	v_pk_fma_f32 v[192:193], v[58:59], v[206:207], v[192:193]
	v_add_f32_dpp v1, v1, v1 row_shr:2 row_mask:0xf bank_mask:0xf bound_ctrl:1
	s_nop 0
	s_nop 0
	v_add_f32_dpp v1, v1, v1 row_shr:4 row_mask:0xf bank_mask:0xf bound_ctrl:1
	s_nop 1
	v_add_f32_dpp v1, v1, v1 row_shr:8 row_mask:0xf bank_mask:0xf bound_ctrl:1
	s_nop 1
	v_mov_b32_dpp v83, v1 row_bcast:15 row_mask:0xa bank_mask:0xf
	v_add_f32_e32 v1, v1, v83
	v_mov_b32_e32 v83, 0
	s_nop 1
	v_mov_b32_dpp v83, v1 row_bcast:31 row_mask:0xc bank_mask:0xf
	v_add_f32_e32 v1, v1, v83
	v_pk_fma_f32 v[192:193], v[64:65], v[200:201], v[192:193]
	ds_read_b128 v[204:207], v88 offset:54272
	v_pk_fma_f32 v[192:193], v[62:63], v[202:203], v[192:193]
	v_readlane_b32 s61, v1, 63
	s_nop 0
	s_nop 0
	s_nop 0
	s_waitcnt lgkmcnt(11)
	v_pk_fma_f32 v[192:193], v[56:57], v[212:213], v[192:193]
	ds_read_b128 v[200:203], v88 offset:55296
	v_pk_fma_f32 v[192:193], v[54:55], v[214:215], v[192:193]
	s_waitcnt lgkmcnt(11)
; #define LAS __attribute__((address_space(3)))
; __device__ __forceinline__ float wave_sum(float v) { return lane63(scan64<false>(v)); }
; template <int YMODE, int EXTRA, bool NORM_OUT, bool XN8  , bool XIN_BF = false  , bool XOUT_BF = false  > ...
;     ...
;                     for (int e = 0; e < 8; ++e) { float s = 0.f;
; #pragma unroll
;                         for (int j = 0; j < 8; ++j) { const f32x4 w = *(const LAS f32x4*)(we + e * D + 256 * j + 4 * F.lane); s += (x[j][0] * w[0] + x[j][1] * w[1]) + (x[j][2] * w[2] + x[j][3] * w[3]); }
;                         d8[e] = wave_sum(s); asm volatile("" ::: "memory"); }
;                     if (EXTRA == 1) {
;                         float v = 0.f;
; #pragma unroll
;                         for (int e = 0; e < 8; ++e) v = (F.lane == e) ? d8[e] : v;
;                         if (F.lane < 8) { const float bb = (F.lane < 4) ? bi[F.lane] : bfg[F.lane - 4]; const float z = 15.f * tanhf((v + bb) * (1.f / 15.f));
;                             const float o = (F.lane < 4) ? z : (fminf(z, 0.f) - log1pf(expf(-fabsf(z)))); gates_out[row * 8 + F.lane] = o; }
	v_pk_fma_f32 v[192:193], v[52:53], v[208:209], v[192:193]
	ds_read_b128 v[212:215], v88 offset:56320
	v_pk_fma_f32 v[192:193], v[50:51], v[210:211], v[192:193]
	s_waitcnt lgkmcnt(11)
	v_pk_fma_f32 v[192:193], v[48:49], v[216:217], v[192:193]
	ds_read_b128 v[208:211], v88 offset:57344
	v_pk_fma_f32 v[192:193], v[46:47], v[218:219], v[192:193]
	s_waitcnt lgkmcnt(11)
	v_pk_fma_f32 v[192:193], v[44:45], v[224:225], v[192:193]
	ds_read_b128 v[216:219], v88 offset:58368
	v_pk_fma_f32 v[192:193], v[42:43], v[226:227], v[192:193]
	s_waitcnt lgkmcnt(11)
	v_pk_fma_f32 v[192:193], v[40:41], v[220:221], v[192:193]
	ds_read_b128 v[224:227], v88 offset:59392
	v_pk_fma_f32 v[192:193], v[38:39], v[222:223], v[192:193]
	s_waitcnt lgkmcnt(11)
	v_pk_fma_f32 v[192:193], v[36:37], v[232:233], v[192:193]
	ds_read_b128 v[220:223], v88 offset:60416
	v_pk_fma_f32 v[192:193], v[34:35], v[234:235], v[192:193]
	v_add_f32_e32 v1, v192, v193
	v_mov_b32_e32 v83, 0
	s_nop 0
	s_nop 0
	v_add_f32_dpp v1, v1, v1 row_shr:1 row_mask:0xf bank_mask:0xf bound_ctrl:1
	s_nop 0
	s_waitcnt lgkmcnt(10)
	v_pk_mul_f32 v[190:191], v[60:61], v[240:241]
	ds_read_b128 v[232:235], v88 offset:61440
	v_pk_fma_f32 v[190:191], v[58:59], v[242:243], v[190:191]
	v_add_f32_dpp v1, v1, v1 row_shr:2 row_mask:0xf bank_mask:0xf bound_ctrl:1
	s_nop 0
	s_nop 0
	v_add_f32_dpp v1, v1, v1 row_shr:4 row_mask:0xf bank_mask:0xf bound_ctrl:1
	s_nop 1
	v_add_f32_dpp v1, v1, v1 row_shr:8 row_mask:0xf bank_mask:0xf bound_ctrl:1
	s_nop 1
	v_mov_b32_dpp v83, v1 row_bcast:15 row_mask:0xa bank_mask:0xf
	v_add_f32_e32 v1, v1, v83
	v_mov_b32_e32 v83, 0
	s_nop 1
	v_mov_b32_dpp v83, v1 row_bcast:31 row_mask:0xc bank_mask:0xf
	v_add_f32_e32 v1, v1, v83
	v_pk_fma_f32 v[190:191], v[64:65], v[228:229], v[190:191]
	ds_read_b128 v[240:243], v88 offset:62464
	v_pk_fma_f32 v[190:191], v[62:63], v[230:231], v[190:191]
	v_readlane_b32 s62, v1, 63
	s_nop 0
	s_nop 0
	s_nop 0
	s_waitcnt lgkmcnt(11)
	v_pk_fma_f32 v[190:191], v[56:57], v[248:249], v[190:191]
	ds_read_b128 v[228:231], v88 offset:63488
	v_pk_fma_f32 v[190:191], v[54:55], v[250:251], v[190:191]
	s_waitcnt lgkmcnt(11)
	v_pk_fma_f32 v[190:191], v[52:53], v[244:245], v[190:191]
	ds_read_b128 v[248:251], v88 offset:64512
	v_pk_fma_f32 v[190:191], v[50:51], v[246:247], v[190:191]
	s_waitcnt lgkmcnt(11)
	v_pk_fma_f32 v[190:191], v[48:49], v[196:197], v[190:191]
	v_pk_fma_f32 v[190:191], v[46:47], v[198:199], v[190:191]
	s_waitcnt lgkmcnt(10)
	v_pk_fma_f32 v[190:191], v[44:45], v[204:205], v[190:191]
	v_pk_fma_f32 v[190:191], v[42:43], v[206:207], v[190:191]
	s_waitcnt lgkmcnt(9)
	v_pk_fma_f32 v[190:191], v[40:41], v[200:201], v[190:191]
	v_pk_fma_f32 v[190:191], v[38:39], v[202:203], v[190:191]
	s_waitcnt lgkmcnt(8)
	v_pk_fma_f32 v[190:191], v[36:37], v[212:213], v[190:191]
	v_pk_fma_f32 v[190:191], v[34:35], v[214:215], v[190:191]
	v_add_f32_e32 v1, v190, v191
	v_mov_b32_e32 v83, 0
	s_nop 0
	s_nop 0
	v_add_f32_dpp v1, v1, v1 row_shr:1 row_mask:0xf bank_mask:0xf bound_ctrl:1
	s_nop 0
	s_waitcnt lgkmcnt(7)
	v_pk_mul_f32 v[192:193], v[64:65], v[208:209]
	v_pk_fma_f32 v[192:193], v[62:63], v[210:211], v[192:193]
	v_add_f32_dpp v1, v1, v1 row_shr:2 row_mask:0xf bank_mask:0xf bound_ctrl:1
	s_waitcnt lgkmcnt(6)
	v_pk_fma_f32 v[192:193], v[60:61], v[216:217], v[192:193]
	v_pk_fma_f32 v[192:193], v[58:59], v[218:219], v[192:193]
	v_add_f32_dpp v1, v1, v1 row_shr:4 row_mask:0xf bank_mask:0xf bound_ctrl:1
	s_nop 0
	s_nop 0
	v_add_f32_dpp v1, v1, v1 row_shr:8 row_mask:0xf bank_mask:0xf bound_ctrl:1
	s_nop 1
	v_mov_b32_dpp v83, v1 row_bcast:15 row_mask:0xa bank_mask:0xf
	v_add_f32_e32 v1, v1, v83
	v_mov_b32_e32 v83, 0
	s_nop 1
	v_mov_b32_dpp v83, v1 row_bcast:31 row_mask:0xc bank_mask:0xf
	v_add_f32_e32 v1, v1, v83
	s_nop 0
	v_readlane_b32 s63, v1, 63
	s_nop 0
	s_nop 0
	s_nop 0
	s_waitcnt lgkmcnt(5)
	v_pk_fma_f32 v[192:193], v[56:57], v[224:225], v[192:193]
	v_pk_fma_f32 v[192:193], v[54:55], v[226:227], v[192:193]
	s_waitcnt lgkmcnt(4)
	v_pk_fma_f32 v[192:193], v[52:53], v[220:221], v[192:193]
	v_pk_fma_f32 v[192:193], v[50:51], v[222:223], v[192:193]
	s_waitcnt lgkmcnt(3)
	v_pk_fma_f32 v[192:193], v[48:49], v[232:233], v[192:193]
	v_pk_fma_f32 v[192:193], v[46:47], v[234:235], v[192:193]
	s_waitcnt lgkmcnt(2)
	v_pk_fma_f32 v[192:193], v[44:45], v[240:241], v[192:193]
	v_pk_fma_f32 v[192:193], v[42:43], v[242:243], v[192:193]
	s_waitcnt lgkmcnt(1)
	v_pk_fma_f32 v[192:193], v[40:41], v[228:229], v[192:193]
	v_pk_fma_f32 v[192:193], v[38:39], v[230:231], v[192:193]
	s_waitcnt lgkmcnt(0)
	v_pk_fma_f32 v[192:193], v[36:37], v[248:249], v[192:193]
	v_pk_fma_f32 v[192:193], v[34:35], v[250:251], v[192:193]
	v_add_f32_e32 v1, v192, v193
	v_mov_b32_e32 v34, 0
	s_nop 0
	v_add_f32_dpp v1, v1, v1 row_shr:1 row_mask:0xf bank_mask:0xf bound_ctrl:1
	s_nop 1
	v_add_f32_dpp v1, v1, v1 row_shr:2 row_mask:0xf bank_mask:0xf bound_ctrl:1
	s_nop 1
	v_add_f32_dpp v1, v1, v1 row_shr:4 row_mask:0xf bank_mask:0xf bound_ctrl:1
	s_nop 1
	v_add_f32_dpp v1, v1, v1 row_shr:8 row_mask:0xf bank_mask:0xf bound_ctrl:1
	s_nop 1
	v_mov_b32_dpp v34, v1 row_bcast:15 row_mask:0xa bank_mask:0xf
	v_add_f32_e32 v1, v1, v34
	v_mov_b32_e32 v34, 0
	s_nop 1
	v_mov_b32_dpp v34, v1 row_bcast:31 row_mask:0xc bank_mask:0xf
	v_add_f32_e32 v1, v1, v34
	s_nop 0
	v_readlane_b32 s64, v1, 63
	s_and_saveexec_b64 s[36:37], s[8:9]
	s_cbranch_execz .LBB0_107
	global_load_dword v1, v[76:77], off
	v_mov_b32_e32 v34, s34
	v_cndmask_b32_e64 v34, 0, v34, s[6:7]
	v_mov_b32_e32 v35, s38
	v_cndmask_b32_e64 v34, v34, v35, s[22:23]
	v_mov_b32_e32 v35, s39
	v_cndmask_b32_e64 v34, v34, v35, s[20:21]
	v_mov_b32_e32 v35, s60
	v_cndmask_b32_e64 v34, v34, v35, s[18:19]
	v_mov_b32_e32 v35, s61
	v_cndmask_b32_e64 v34, v34, v35, s[16:17]
	v_mov_b32_e32 v35, s62
	v_cndmask_b32_e64 v34, v34, v35, s[14:15]
	v_mov_b32_e32 v35, s63
	v_cndmask_b32_e64 v34, v34, v35, s[12:13]
	v_mov_b32_e32 v35, s64
	v_cndmask_b32_e64 v34, v34, v35, s[10:11]
	s_waitcnt vmcnt(0) lgkmcnt(0)
	v_add_f32_e32 v1, v34, v1
	v_mul_f32_e32 v1, 0x3d888889, v1
	v_cmp_nlt_f32_e64 s[38:39], |v1|, s43
	s_and_saveexec_b64 s[60:61], s[38:39]
	s_xor_b64 s[38:39], exec, s[60:61]
	s_cbranch_execz .LBB0_115
	v_add_f32_e64 v34, |v1|, |v1|
	v_mul_f32_e32 v35, 0x3fb8aa3b, v34
	v_rndne_f32_e32 v36, v35
	v_sub_f32_e32 v37, v35, v36
	v_fma_f32 v35, v34, s44, -v35
	v_fmac_f32_e32 v35, 0x32a5705f, v34
	v_add_f32_e32 v35, v37, v35
	v_cvt_i32_f32_e32 v36, v36
	v_exp_f32_e32 v35, v35
	v_cmp_ngt_f32_e32 vcc, s45, v34
	v_ldexp_f32 v35, v35, v36
	s_nop 0
	v_cndmask_b32_e32 v35, 0, v35, vcc
	v_cmp_nlt_f32_e32 vcc, s46, v34
	s_nop 1
	v_cndmask_b32_e32 v34, v94, v35, vcc
	v_add_f32_e32 v34, 1.0, v34
	v_rcp_f32_e32 v34, v34
	s_nop 0
	v_fma_f32 v34, v34, -2.0, 1.0

; #define LAS __attribute__((address_space(3)))
; __device__ __forceinline__ unsigned cvtpk(float lo, float hi) { f32x2 v = {lo, hi}; bf16x2_t b = __builtin_convertvector(v, bf16x2_t); return __builtin_bit_cast(unsigned, b); }
; __device__ __forceinline__ float wave_max(float v) { return lane63(scan64<true>(v)); }
; template <int YMODE, int EXTRA, bool NORM_OUT, bool XN8  , bool XIN_BF = false  , bool XOUT_BF = false  > ...
;     ...
;                 if (XN8) {
;                     float am = 0.f;
; #pragma unroll
;                     for (int j = 0; j < 8; ++j) am = fmaxf(fmaxf(am, fmaxf(fabsf(x[j][0]), fabsf(x[j][1]))), fmaxf(fabsf(x[j][2]), fabsf(x[j][3])));
;                     am = wave_max(am);
;                     const float inv = am > 0.f ? 127.f / am : 0.f;
;                     if (F.lane == 0) { rowmax[row] = am; if (EXTRA == 2) route[384 + rl] = am; }
; #pragma unroll
;                     for (int j = 0; j < 8; ++j) *(unsigned*)((unsigned char*)XN + row * D + 256 * j + 4 * F.lane) = pack_i8x4(x[j][0] * inv, x[j][1] * inv, x[j][2] * inv, x[j][3] * inv);
;                 } else {
; #pragma unroll
;                     for (int j = 0; j < 8; ++j) { u32x2 w; w.x = cvtpk(x[j][0], x[j][1]); w.y = cvtpk(x[j][2], x[j][3]); *(u32x2*)(XN + row * D + 256 * j + 4 * F.lane) = w; }
;                 }
;                 if (EXTRA) {
;                     float d8[8];
; #pragma unroll
;                     for (int e = 0; e < 8; ++e) { float s = 0.f;
; #pragma unroll
;                         for (int j = 0; j < 8; ++j) { const f32x4 w = *(const LAS f32x4*)(we + e * D + 256 * j + 4 * F.lane); s += (x[j][0] * w[0] + x[j][1] * w[1]) + (x[j][2] * w[2] + x[j][3] * w[3]); }
.LBB0_1311:
	s_or_b64 exec, exec, s[26:27]
	ds_read_b128 v[196:199], v105
	ds_read_b128 v[200:203], v105 offset:1024
	ds_read_b128 v[204:207], v105 offset:2048
	ds_read_b128 v[208:211], v105 offset:3072
	ds_read_b128 v[212:215], v105 offset:4096
	ds_read_b128 v[216:219], v105 offset:5120
	ds_read_b128 v[220:223], v105 offset:6144
	ds_read_b128 v[224:227], v105 offset:7168
	ds_read_b128 v[228:231], v105 offset:8192
	ds_read_b128 v[232:235], v105 offset:9216
	ds_read_b128 v[240:243], v105 offset:10240
	ds_read_b128 v[244:247], v105 offset:11264
	v_div_scale_f32 v1, s[26:27], s34, s34, v110
	v_rcp_f32_e32 v25, v1
	v_mov_b32_e32 v90, s34
	s_mov_b32 s26, 0x42fe0000
	v_div_scale_f32 v90, vcc, s26, v90, s26
	v_fma_f32 v91, -v1, v25, 1.0
	v_fmac_f32_e32 v25, v91, v25
	v_mul_f32_e32 v91, v90, v25
	v_fma_f32 v92, -v1, v91, v90
	v_fmac_f32_e32 v91, v92, v25
	v_fma_f32 v1, -v1, v91, v90
	v_div_fmas_f32 v1, v1, v25, v91
	v_div_fixup_f32 v1, v1, s34, v110
	v_cmp_gt_f32_e64 vcc, s34, 0
	s_lshl_b64 s[26:27], s[36:37], 11
	v_lshl_add_u64 v[94:95], v[22:23], 0, s[26:27]
	v_cndmask_b32_e32 v1, 0, v1, vcc
	v_mul_f32_e32 v90, v85, v1
	v_mul_f32_e32 v25, v84, v1
	v_mul_f32_e32 v91, v72, v1
	v_mul_f32_e32 v92, v73, v1
	v_med3_f32 v90, v90, s42, v110
	v_med3_f32 v25, v25, s42, v110
	v_rndne_f32_e32 v90, v90
	v_med3_f32 v91, v91, s42, v110
	v_med3_f32 v92, v92, s42, v110
	v_rndne_f32_e32 v25, v25
	v_cvt_i32_f32_e32 v90, v90
	v_rndne_f32_e32 v91, v91
	v_rndne_f32_e32 v92, v92
	v_cvt_i32_f32_e32 v25, v25
	v_cvt_i32_f32_sdwa v91, v91 dst_sel:WORD_1 dst_unused:UNUSED_PAD src0_sel:DWORD
	v_cvt_i32_f32_e32 v92, v92
	v_lshlrev_b32_e32 v90, 8, v90
	v_and_b32_e32 v90, 0xff00, v90
	v_and_b32_e32 v91, 0xff0000, v91
	v_perm_b32 v25, v92, v25, s43
	v_or3_b32 v25, v25, v90, v91
	v_mul_f32_e32 v90, v89, v1
	global_store_dword v[94:95], v25, off
	v_mul_f32_e32 v25, v88, v1
	v_mul_f32_e32 v91, v62, v1
	v_mul_f32_e32 v92, v63, v1
	v_med3_f32 v90, v90, s42, v110
	v_med3_f32 v25, v25, s42, v110
	v_rndne_f32_e32 v90, v90
	v_med3_f32 v91, v91, s42, v110
	v_med3_f32 v92, v92, s42, v110
	v_rndne_f32_e32 v25, v25
	v_cvt_i32_f32_e32 v90, v90
	v_rndne_f32_e32 v91, v91
	v_rndne_f32_e32 v92, v92
	v_cvt_i32_f32_e32 v25, v25
	v_cvt_i32_f32_sdwa v91, v91 dst_sel:WORD_1 dst_unused:UNUSED_PAD src0_sel:DWORD
	v_cvt_i32_f32_e32 v92, v92
	v_lshlrev_b32_e32 v90, 8, v90
	v_and_b32_e32 v90, 0xff00, v90
	v_and_b32_e32 v91, 0xff0000, v91
	v_perm_b32 v25, v92, v25, s43
	v_or3_b32 v25, v25, v90, v91
	v_mul_f32_e32 v90, v81, v1
	global_store_dword v[94:95], v25, off offset:256
	v_mul_f32_e32 v25, v80, v1
	v_mul_f32_e32 v91, v70, v1
	v_mul_f32_e32 v92, v71, v1
	v_med3_f32 v90, v90, s42, v110
	v_med3_f32 v25, v25, s42, v110
	v_rndne_f32_e32 v90, v90
	v_med3_f32 v91, v91, s42, v110
	v_med3_f32 v92, v92, s42, v110
	v_rndne_f32_e32 v25, v25
	v_cvt_i32_f32_e32 v90, v90
	v_rndne_f32_e32 v91, v91
	v_rndne_f32_e32 v92, v92
	v_cvt_i32_f32_e32 v25, v25
	v_cvt_i32_f32_sdwa v91, v91 dst_sel:WORD_1 dst_unused:UNUSED_PAD src0_sel:DWORD
	v_cvt_i32_f32_e32 v92, v92
	v_lshlrev_b32_e32 v90, 8, v90
	v_and_b32_e32 v90, 0xff00, v90
	v_and_b32_e32 v91, 0xff0000, v91
	v_perm_b32 v25, v92, v25, s43
	v_or3_b32 v25, v25, v90, v91
	v_mul_f32_e32 v90, v87, v1
	global_store_dword v[94:95], v25, off offset:512
	v_mul_f32_e32 v25, v86, v1
	v_mul_f32_e32 v91, v60, v1
	v_mul_f32_e32 v92, v61, v1
	v_med3_f32 v90, v90, s42, v110
	v_med3_f32 v25, v25, s42, v110
	v_rndne_f32_e32 v90, v90
	v_med3_f32 v91, v91, s42, v110
	v_med3_f32 v92, v92, s42, v110
	v_rndne_f32_e32 v25, v25
	v_cvt_i32_f32_e32 v90, v90
	v_rndne_f32_e32 v91, v91
	v_rndne_f32_e32 v92, v92
	v_cvt_i32_f32_e32 v25, v25
	v_cvt_i32_f32_sdwa v91, v91 dst_sel:WORD_1 dst_unused:UNUSED_PAD src0_sel:DWORD
	v_cvt_i32_f32_e32 v92, v92
	v_lshlrev_b32_e32 v90, 8, v90
	v_and_b32_e32 v90, 0xff00, v90
	v_and_b32_e32 v91, 0xff0000, v91
	v_perm_b32 v25, v92, v25, s43
	v_or3_b32 v25, v25, v90, v91
	v_mul_f32_e32 v90, v77, v1
	global_store_dword v[94:95], v25, off offset:768
	v_mul_f32_e32 v25, v76, v1
	v_mul_f32_e32 v91, v68, v1
	v_mul_f32_e32 v92, v69, v1
	v_med3_f32 v90, v90, s42, v110
	v_med3_f32 v25, v25, s42, v110
	v_rndne_f32_e32 v90, v90
	v_med3_f32 v91, v91, s42, v110
	v_med3_f32 v92, v92, s42, v110
	v_rndne_f32_e32 v25, v25
	v_cvt_i32_f32_e32 v90, v90
	v_rndne_f32_e32 v91, v91
	v_rndne_f32_e32 v92, v92
	v_cvt_i32_f32_e32 v25, v25
	v_cvt_i32_f32_sdwa v91, v91 dst_sel:WORD_1 dst_unused:UNUSED_PAD src0_sel:DWORD
	v_cvt_i32_f32_e32 v92, v92
	v_lshlrev_b32_e32 v90, 8, v90
	v_and_b32_e32 v90, 0xff00, v90
	v_and_b32_e32 v91, 0xff0000, v91
	v_perm_b32 v25, v92, v25, s43
	v_or3_b32 v25, v25, v90, v91
	v_mul_f32_e32 v90, v83, v1
	global_store_dword v[94:95], v25, off offset:1024
	v_mul_f32_e32 v25, v82, v1
	v_mul_f32_e32 v91, v58, v1
	v_mul_f32_e32 v92, v59, v1
	v_med3_f32 v90, v90, s42, v110
	v_med3_f32 v25, v25, s42, v110
	v_rndne_f32_e32 v90, v90
	v_med3_f32 v91, v91, s42, v110
	v_med3_f32 v92, v92, s42, v110
	v_rndne_f32_e32 v25, v25
	v_cvt_i32_f32_e32 v90, v90
	v_rndne_f32_e32 v91, v91
	v_rndne_f32_e32 v92, v92
	v_cvt_i32_f32_e32 v25, v25
	v_cvt_i32_f32_sdwa v91, v91 dst_sel:WORD_1 dst_unused:UNUSED_PAD src0_sel:DWORD
	v_cvt_i32_f32_e32 v92, v92
	v_lshlrev_b32_e32 v90, 8, v90
	v_and_b32_e32 v90, 0xff00, v90
	v_and_b32_e32 v91, 0xff0000, v91
	v_perm_b32 v25, v92, v25, s43
	v_or3_b32 v25, v25, v90, v91
	v_mul_f32_e32 v90, v75, v1
	global_store_dword v[94:95], v25, off offset:1280
	v_mul_f32_e32 v25, v74, v1
	v_mul_f32_e32 v91, v64, v1
	v_mul_f32_e32 v92, v65, v1
	v_med3_f32 v90, v90, s42, v110
	v_med3_f32 v25, v25, s42, v110
	v_rndne_f32_e32 v90, v90
	v_med3_f32 v91, v91, s42, v110
	v_med3_f32 v92, v92, s42, v110
	v_rndne_f32_e32 v25, v25
	v_cvt_i32_f32_e32 v90, v90
	v_rndne_f32_e32 v91, v91
	v_rndne_f32_e32 v92, v92
	v_cvt_i32_f32_e32 v25, v25
	v_cvt_i32_f32_sdwa v91, v91 dst_sel:WORD_1 dst_unused:UNUSED_PAD src0_sel:DWORD
	v_cvt_i32_f32_e32 v92, v92
	v_lshlrev_b32_e32 v90, 8, v90
	v_and_b32_e32 v90, 0xff00, v90
	v_and_b32_e32 v91, 0xff0000, v91
	v_perm_b32 v25, v92, v25, s43
	v_or3_b32 v25, v25, v90, v91
	v_mul_f32_e32 v90, v79, v1
	global_store_dword v[94:95], v25, off offset:1536
	v_mul_f32_e32 v25, v78, v1
	v_mul_f32_e32 v91, v66, v1
	v_mul_f32_e32 v1, v67, v1
	v_med3_f32 v90, v90, s42, v110
	v_med3_f32 v25, v25, s42, v110
	v_rndne_f32_e32 v90, v90
	v_med3_f32 v91, v91, s42, v110
	v_med3_f32 v1, v1, s42, v110
	v_rndne_f32_e32 v25, v25
	v_cvt_i32_f32_e32 v90, v90
	v_rndne_f32_e32 v91, v91
	v_rndne_f32_e32 v1, v1
	v_cvt_i32_f32_e32 v25, v25
	v_cvt_i32_f32_sdwa v91, v91 dst_sel:WORD_1 dst_unused:UNUSED_PAD src0_sel:DWORD
	v_cvt_i32_f32_e32 v1, v1
	v_lshlrev_b32_e32 v90, 8, v90
	v_and_b32_e32 v96, 0xff00, v90
	v_and_b32_e32 v97, 0xff0000, v91
	s_nop 0
	v_perm_b32 v1, v1, v25, s43
	v_or3_b32 v1, v1, v96, v97
	global_store_dword v[94:95], v1, off offset:1792
	s_nop 0
	s_waitcnt lgkmcnt(12)
; #define LAS __attribute__((address_space(3)))
; __device__ __forceinline__ float wave_sum(float v) { return lane63(scan64<false>(v)); }
; template <int YMODE, int EXTRA, bool NORM_OUT, bool XN8  , bool XIN_BF = false  , bool XOUT_BF = false  > ...
;     ...
;                     for (int e = 0; e < 8; ++e) { float s = 0.f;
; #pragma unroll
;                         for (int j = 0; j < 8; ++j) { const f32x4 w = *(const LAS f32x4*)(we + e * D + 256 * j + 4 * F.lane); s += (x[j][0] * w[0] + x[j][1] * w[1]) + (x[j][2] * w[2] + x[j][3] * w[3]); }
;                         d8[e] = wave_sum(s); asm volatile("" ::: "memory"); }
	s_waitcnt lgkmcnt(11)
	v_pk_mul_f32 v[190:191], v[84:85], v[196:197]
	ds_read_b128 v[248:251], v105 offset:12288
	v_pk_fma_f32 v[190:191], v[72:73], v[198:199], v[190:191]
	s_waitcnt lgkmcnt(11)
	v_pk_fma_f32 v[190:191], v[88:89], v[200:201], v[190:191]
	ds_read_b128 v[196:199], v105 offset:13312
	v_pk_fma_f32 v[190:191], v[62:63], v[202:203], v[190:191]
	s_waitcnt lgkmcnt(11)
	v_pk_fma_f32 v[190:191], v[80:81], v[204:205], v[190:191]
	ds_read_b128 v[200:203], v105 offset:14336
	v_pk_fma_f32 v[190:191], v[70:71], v[206:207], v[190:191]
	s_waitcnt lgkmcnt(11)
	v_pk_fma_f32 v[190:191], v[86:87], v[208:209], v[190:191]
	ds_read_b128 v[204:207], v105 offset:15360
	v_pk_fma_f32 v[190:191], v[60:61], v[210:211], v[190:191]
	s_waitcnt lgkmcnt(11)
	v_pk_fma_f32 v[190:191], v[76:77], v[212:213], v[190:191]
	ds_read_b128 v[208:211], v105 offset:16384
	v_pk_fma_f32 v[190:191], v[68:69], v[214:215], v[190:191]
	s_waitcnt lgkmcnt(11)
	v_pk_fma_f32 v[190:191], v[82:83], v[216:217], v[190:191]
	ds_read_b128 v[212:215], v105 offset:17408
	v_pk_fma_f32 v[190:191], v[58:59], v[218:219], v[190:191]
	s_waitcnt lgkmcnt(11)
	v_pk_fma_f32 v[190:191], v[74:75], v[220:221], v[190:191]
	ds_read_b128 v[216:219], v105 offset:18432
	v_pk_fma_f32 v[190:191], v[64:65], v[222:223], v[190:191]
	s_waitcnt lgkmcnt(11)
	v_pk_fma_f32 v[190:191], v[78:79], v[224:225], v[190:191]
	ds_read_b128 v[220:223], v105 offset:19456
	v_pk_fma_f32 v[190:191], v[66:67], v[226:227], v[190:191]
	v_add_f32_e32 v1, v190, v191
	v_mov_b32_e32 v25, 0
	s_nop 0
	s_nop 0
	v_add_f32_dpp v1, v1, v1 row_shr:1 row_mask:0xf bank_mask:0xf bound_ctrl:1
	s_nop 1
	v_add_f32_dpp v1, v1, v1 row_shr:2 row_mask:0xf bank_mask:0xf bound_ctrl:1
	s_nop 1
	v_add_f32_dpp v1, v1, v1 row_shr:4 row_mask:0xf bank_mask:0xf bound_ctrl:1
	s_nop 1
	v_add_f32_dpp v1, v1, v1 row_shr:8 row_mask:0xf bank_mask:0xf bound_ctrl:1
	s_nop 1
	v_mov_b32_dpp v25, v1 row_bcast:15 row_mask:0xa bank_mask:0xf
	v_add_f32_e32 v1, v1, v25
	v_mov_b32_e32 v25, 0
	s_nop 1
	v_mov_b32_dpp v25, v1 row_bcast:31 row_mask:0xc bank_mask:0xf
	v_add_f32_e32 v1, v1, v25
	s_nop 0
	s_waitcnt lgkmcnt(11)
	v_pk_mul_f32 v[192:193], v[84:85], v[228:229]
	ds_read_b128 v[224:227], v105 offset:20480
	v_pk_fma_f32 v[192:193], v[72:73], v[230:231], v[192:193]
	v_readlane_b32 s34, v1, 63
	s_nop 0
	s_nop 0
	s_waitcnt lgkmcnt(11)
	v_pk_fma_f32 v[192:193], v[88:89], v[232:233], v[192:193]
	ds_read_b128 v[228:231], v105 offset:21504
	v_pk_fma_f32 v[192:193], v[62:63], v[234:235], v[192:193]
	s_waitcnt lgkmcnt(11)
	v_pk_fma_f32 v[192:193], v[80:81], v[240:241], v[192:193]
	ds_read_b128 v[232:235], v105 offset:22528
	v_pk_fma_f32 v[192:193], v[70:71], v[242:243], v[192:193]
	s_waitcnt lgkmcnt(11)
	v_pk_fma_f32 v[192:193], v[86:87], v[244:245], v[192:193]
	ds_read_b128 v[240:243], v105 offset:23552
	v_pk_fma_f32 v[192:193], v[60:61], v[246:247], v[192:193]
	s_waitcnt lgkmcnt(11)
	v_pk_fma_f32 v[192:193], v[76:77], v[248:249], v[192:193]
	ds_read_b128 v[244:247], v105 offset:24576
	v_pk_fma_f32 v[192:193], v[68:69], v[250:251], v[192:193]
	s_waitcnt lgkmcnt(11)
	v_pk_fma_f32 v[192:193], v[82:83], v[196:197], v[192:193]
	ds_read_b128 v[248:251], v105 offset:25600
	v_pk_fma_f32 v[192:193], v[58:59], v[198:199], v[192:193]
	s_waitcnt lgkmcnt(11)
	v_pk_fma_f32 v[192:193], v[74:75], v[200:201], v[192:193]
	ds_read_b128 v[196:199], v105 offset:26624
	v_pk_fma_f32 v[192:193], v[64:65], v[202:203], v[192:193]
	s_waitcnt lgkmcnt(11)
	v_pk_fma_f32 v[192:193], v[78:79], v[204:205], v[192:193]
	ds_read_b128 v[200:203], v105 offset:27648
	v_pk_fma_f32 v[192:193], v[66:67], v[206:207], v[192:193]
	v_add_f32_e32 v1, v192, v193
	v_mov_b32_e32 v25, 0
	s_nop 0
	s_nop 0
	v_add_f32_dpp v1, v1, v1 row_shr:1 row_mask:0xf bank_mask:0xf bound_ctrl:1
	s_nop 1
	v_add_f32_dpp v1, v1, v1 row_shr:2 row_mask:0xf bank_mask:0xf bound_ctrl:1
	s_nop 1
	v_add_f32_dpp v1, v1, v1 row_shr:4 row_mask:0xf bank_mask:0xf bound_ctrl:1
	s_nop 1
	v_add_f32_dpp v1, v1, v1 row_shr:8 row_mask:0xf bank_mask:0xf bound_ctrl:1
	s_nop 1
	v_mov_b32_dpp v25, v1 row_bcast:15 row_mask:0xa bank_mask:0xf
	v_add_f32_e32 v1, v1, v25
	v_mov_b32_e32 v25, 0
	s_nop 1
	v_mov_b32_dpp v25, v1 row_bcast:31 row_mask:0xc bank_mask:0xf
	v_add_f32_e32 v1, v1, v25
	s_nop 0
	s_waitcnt lgkmcnt(11)
	v_pk_mul_f32 v[190:191], v[84:85], v[208:209]
	ds_read_b128 v[204:207], v105 offset:28672
	v_pk_fma_f32 v[190:191], v[72:73], v[210:211], v[190:191]
	v_readlane_b32 s38, v1, 63
	s_nop 0
	s_nop 0
	s_waitcnt lgkmcnt(11)
	v_pk_fma_f32 v[190:191], v[88:89], v[212:213], v[190:191]
	ds_read_b128 v[208:211], v105 offset:29696
	v_pk_fma_f32 v[190:191], v[62:63], v[214:215], v[190:191]
	s_waitcnt lgkmcnt(11)
	v_pk_fma_f32 v[190:191], v[80:81], v[216:217], v[190:191]
	ds_read_b128 v[212:215], v105 offset:30720
	v_pk_fma_f32 v[190:191], v[70:71], v[218:219], v[190:191]
	s_waitcnt lgkmcnt(11)
	v_pk_fma_f32 v[190:191], v[86:87], v[220:221], v[190:191]
	ds_read_b128 v[216:219], v105 offset:31744
	v_pk_fma_f32 v[190:191], v[60:61], v[222:223], v[190:191]
	s_waitcnt lgkmcnt(11)
	v_pk_fma_f32 v[190:191], v[76:77], v[224:225], v[190:191]
	ds_read_b128 v[220:223], v105 offset:32768
	v_pk_fma_f32 v[190:191], v[68:69], v[226:227], v[190:191]
	s_waitcnt lgkmcnt(11)
	v_pk_fma_f32 v[190:191], v[82:83], v[228:229], v[190:191]
	ds_read_b128 v[224:227], v105 offset:33792
	v_pk_fma_f32 v[190:191], v[58:59], v[230:231], v[190:191]
	s_waitcnt lgkmcnt(11)
	v_pk_fma_f32 v[190:191], v[74:75], v[232:233], v[190:191]
	ds_read_b128 v[228:231], v105 offset:34816
	v_pk_fma_f32 v[190:191], v[64:65], v[234:235], v[190:191]
	s_waitcnt lgkmcnt(11)
; #define LAS __attribute__((address_space(3)))
; __device__ __forceinline__ float wave_sum(float v) { return lane63(scan64<false>(v)); }
; template <int YMODE, int EXTRA, bool NORM_OUT, bool XN8  , bool XIN_BF = false  , bool XOUT_BF = false  > ...
;     ...
;                     for (int e = 0; e < 8; ++e) { float s = 0.f;
; #pragma unroll
;                         for (int j = 0; j < 8; ++j) { const f32x4 w = *(const LAS f32x4*)(we + e * D + 256 * j + 4 * F.lane); s += (x[j][0] * w[0] + x[j][1] * w[1]) + (x[j][2] * w[2] + x[j][3] * w[3]); }
;                         d8[e] = wave_sum(s); asm volatile("" ::: "memory"); }
	v_pk_fma_f32 v[190:191], v[78:79], v[240:241], v[190:191]
	ds_read_b128 v[232:235], v105 offset:35840
	v_pk_fma_f32 v[190:191], v[66:67], v[242:243], v[190:191]
	v_add_f32_e32 v1, v190, v191
	v_mov_b32_e32 v25, 0
	s_nop 0
	s_nop 0
	v_add_f32_dpp v1, v1, v1 row_shr:1 row_mask:0xf bank_mask:0xf bound_ctrl:1
	s_nop 1
	v_add_f32_dpp v1, v1, v1 row_shr:2 row_mask:0xf bank_mask:0xf bound_ctrl:1
	s_nop 1
	v_add_f32_dpp v1, v1, v1 row_shr:4 row_mask:0xf bank_mask:0xf bound_ctrl:1
	s_nop 1
	v_add_f32_dpp v1, v1, v1 row_shr:8 row_mask:0xf bank_mask:0xf bound_ctrl:1
	s_nop 1
	v_mov_b32_dpp v25, v1 row_bcast:15 row_mask:0xa bank_mask:0xf
	v_add_f32_e32 v1, v1, v25
	v_mov_b32_e32 v25, 0
	s_nop 1
	v_mov_b32_dpp v25, v1 row_bcast:31 row_mask:0xc bank_mask:0xf
	v_add_f32_e32 v1, v1, v25
	s_nop 0
	s_waitcnt lgkmcnt(11)
	v_pk_mul_f32 v[192:193], v[84:85], v[244:245]
	ds_read_b128 v[240:243], v105 offset:36864
	v_pk_fma_f32 v[192:193], v[72:73], v[246:247], v[192:193]
	v_readlane_b32 s39, v1, 63
	s_nop 0
	s_nop 0
	s_waitcnt lgkmcnt(11)
	v_pk_fma_f32 v[192:193], v[88:89], v[248:249], v[192:193]
	ds_read_b128 v[244:247], v105 offset:37888
	v_pk_fma_f32 v[192:193], v[62:63], v[250:251], v[192:193]
	s_waitcnt lgkmcnt(11)
	v_pk_fma_f32 v[192:193], v[80:81], v[196:197], v[192:193]
	ds_read_b128 v[248:251], v105 offset:38912
	v_pk_fma_f32 v[192:193], v[70:71], v[198:199], v[192:193]
	s_waitcnt lgkmcnt(11)
	v_pk_fma_f32 v[192:193], v[86:87], v[200:201], v[192:193]
	ds_read_b128 v[196:199], v105 offset:39936
	v_pk_fma_f32 v[192:193], v[60:61], v[202:203], v[192:193]
	s_waitcnt lgkmcnt(11)
	v_pk_fma_f32 v[192:193], v[76:77], v[204:205], v[192:193]
	ds_read_b128 v[200:203], v105 offset:40960
	v_pk_fma_f32 v[192:193], v[68:69], v[206:207], v[192:193]
	s_waitcnt lgkmcnt(11)
	v_pk_fma_f32 v[192:193], v[82:83], v[208:209], v[192:193]
	ds_read_b128 v[204:207], v105 offset:41984
	v_pk_fma_f32 v[192:193], v[58:59], v[210:211], v[192:193]
	s_waitcnt lgkmcnt(11)
	v_pk_fma_f32 v[192:193], v[74:75], v[212:213], v[192:193]
	ds_read_b128 v[208:211], v105 offset:43008
	v_pk_fma_f32 v[192:193], v[64:65], v[214:215], v[192:193]
	s_waitcnt lgkmcnt(11)
	v_pk_fma_f32 v[192:193], v[78:79], v[216:217], v[192:193]
	ds_read_b128 v[212:215], v105 offset:44032
	v_pk_fma_f32 v[192:193], v[66:67], v[218:219], v[192:193]
	v_add_f32_e32 v1, v192, v193
	v_mov_b32_e32 v25, 0
	s_nop 0
	s_nop 0
	v_add_f32_dpp v1, v1, v1 row_shr:1 row_mask:0xf bank_mask:0xf bound_ctrl:1
	s_nop 1
	v_add_f32_dpp v1, v1, v1 row_shr:2 row_mask:0xf bank_mask:0xf bound_ctrl:1
	s_nop 1
	v_add_f32_dpp v1, v1, v1 row_shr:4 row_mask:0xf bank_mask:0xf bound_ctrl:1
	s_nop 1
	v_add_f32_dpp v1, v1, v1 row_shr:8 row_mask:0xf bank_mask:0xf bound_ctrl:1
	s_nop 1
	v_mov_b32_dpp v25, v1 row_bcast:15 row_mask:0xa bank_mask:0xf
	v_add_f32_e32 v1, v1, v25
	v_mov_b32_e32 v25, 0
	s_nop 1
	v_mov_b32_dpp v25, v1 row_bcast:31 row_mask:0xc bank_mask:0xf
	v_add_f32_e32 v1, v1, v25
	s_nop 0
	s_waitcnt lgkmcnt(11)
	v_pk_mul_f32 v[190:191], v[84:85], v[220:221]
	ds_read_b128 v[216:219], v105 offset:45056
	v_pk_fma_f32 v[190:191], v[72:73], v[222:223], v[190:191]
	v_readlane_b32 s62, v1, 63
	s_nop 0
	s_nop 0
	s_waitcnt lgkmcnt(11)
	v_pk_fma_f32 v[190:191], v[88:89], v[224:225], v[190:191]
	ds_read_b128 v[220:223], v105 offset:46080
	v_pk_fma_f32 v[190:191], v[62:63], v[226:227], v[190:191]
	s_waitcnt lgkmcnt(11)
	v_pk_fma_f32 v[190:191], v[80:81], v[228:229], v[190:191]
	ds_read_b128 v[224:227], v105 offset:47104
	v_pk_fma_f32 v[190:191], v[70:71], v[230:231], v[190:191]
	s_waitcnt lgkmcnt(11)
	v_pk_fma_f32 v[190:191], v[86:87], v[232:233], v[190:191]
	ds_read_b128 v[228:231], v105 offset:48128
	v_pk_fma_f32 v[190:191], v[60:61], v[234:235], v[190:191]
	s_waitcnt lgkmcnt(11)
	v_pk_fma_f32 v[190:191], v[76:77], v[240:241], v[190:191]
	ds_read_b128 v[232:235], v105 offset:49152
	v_pk_fma_f32 v[190:191], v[68:69], v[242:243], v[190:191]
	s_waitcnt lgkmcnt(11)
	v_pk_fma_f32 v[190:191], v[82:83], v[244:245], v[190:191]
	ds_read_b128 v[240:243], v105 offset:50176
	v_pk_fma_f32 v[190:191], v[58:59], v[246:247], v[190:191]
	s_waitcnt lgkmcnt(11)
	v_pk_fma_f32 v[190:191], v[74:75], v[248:249], v[190:191]
	ds_read_b128 v[244:247], v105 offset:51200
	v_pk_fma_f32 v[190:191], v[64:65], v[250:251], v[190:191]
	s_waitcnt lgkmcnt(11)
	v_pk_fma_f32 v[190:191], v[78:79], v[196:197], v[190:191]
	ds_read_b128 v[248:251], v105 offset:52224
	v_pk_fma_f32 v[190:191], v[66:67], v[198:199], v[190:191]
	v_add_f32_e32 v1, v190, v191
	v_mov_b32_e32 v25, 0
	s_nop 0
	s_nop 0
	v_add_f32_dpp v1, v1, v1 row_shr:1 row_mask:0xf bank_mask:0xf bound_ctrl:1
	s_nop 1
	v_add_f32_dpp v1, v1, v1 row_shr:2 row_mask:0xf bank_mask:0xf bound_ctrl:1
	s_nop 1
	v_add_f32_dpp v1, v1, v1 row_shr:4 row_mask:0xf bank_mask:0xf bound_ctrl:1
	s_nop 1
	v_add_f32_dpp v1, v1, v1 row_shr:8 row_mask:0xf bank_mask:0xf bound_ctrl:1
	s_nop 1
	v_mov_b32_dpp v25, v1 row_bcast:15 row_mask:0xa bank_mask:0xf
	v_add_f32_e32 v1, v1, v25
	v_mov_b32_e32 v25, 0
	s_nop 1
	v_mov_b32_dpp v25, v1 row_bcast:31 row_mask:0xc bank_mask:0xf
	v_add_f32_e32 v1, v1, v25
	s_nop 0
	s_waitcnt lgkmcnt(11)
	v_pk_mul_f32 v[192:193], v[84:85], v[200:201]
	ds_read_b128 v[196:199], v105 offset:53248
	v_pk_fma_f32 v[192:193], v[72:73], v[202:203], v[192:193]
	v_readlane_b32 s63, v1, 63
	s_nop 0
	s_nop 0
	s_waitcnt lgkmcnt(11)
	v_pk_fma_f32 v[192:193], v[88:89], v[204:205], v[192:193]
	ds_read_b128 v[200:203], v105 offset:54272
	v_pk_fma_f32 v[192:193], v[62:63], v[206:207], v[192:193]
	s_waitcnt lgkmcnt(11)
	v_pk_fma_f32 v[192:193], v[80:81], v[208:209], v[192:193]
	ds_read_b128 v[204:207], v105 offset:55296
	v_pk_fma_f32 v[192:193], v[70:71], v[210:211], v[192:193]
	s_waitcnt lgkmcnt(11)
; #define LAS __attribute__((address_space(3)))
; __device__ __forceinline__ float wave_sum(float v) { return lane63(scan64<false>(v)); }
; template <int YMODE, int EXTRA, bool NORM_OUT, bool XN8  , bool XIN_BF = false  , bool XOUT_BF = false  > ...
;     ...
;                     for (int e = 0; e < 8; ++e) { float s = 0.f;
; #pragma unroll
;                         for (int j = 0; j < 8; ++j) { const f32x4 w = *(const LAS f32x4*)(we + e * D + 256 * j + 4 * F.lane); s += (x[j][0] * w[0] + x[j][1] * w[1]) + (x[j][2] * w[2] + x[j][3] * w[3]); }
;                         d8[e] = wave_sum(s); asm volatile("" ::: "memory"); }
;                     if (EXTRA == 1) {
;                         float v = 0.f;
; #pragma unroll
;                         for (int e = 0; e < 8; ++e) v = (F.lane == e) ? d8[e] : v;
;                         if (F.lane < 8) { const float bb = (F.lane < 4) ? bi[F.lane] : bfg[F.lane - 4]; const float z = 15.f * tanhf((v + bb) * (1.f / 15.f));
;                             const float o = (F.lane < 4) ? z : (fminf(z, 0.f) - log1pf(expf(-fabsf(z)))); gates_out[row * 8 + F.lane] = o; }
	v_pk_fma_f32 v[192:193], v[86:87], v[212:213], v[192:193]
	ds_read_b128 v[208:211], v105 offset:56320
	v_pk_fma_f32 v[192:193], v[60:61], v[214:215], v[192:193]
	s_waitcnt lgkmcnt(11)
	v_pk_fma_f32 v[192:193], v[76:77], v[216:217], v[192:193]
	ds_read_b128 v[212:215], v105 offset:57344
	v_pk_fma_f32 v[192:193], v[68:69], v[218:219], v[192:193]
	s_waitcnt lgkmcnt(11)
	v_pk_fma_f32 v[192:193], v[82:83], v[220:221], v[192:193]
	ds_read_b128 v[216:219], v105 offset:58368
	v_pk_fma_f32 v[192:193], v[58:59], v[222:223], v[192:193]
	s_waitcnt lgkmcnt(11)
	v_pk_fma_f32 v[192:193], v[74:75], v[224:225], v[192:193]
	ds_read_b128 v[220:223], v105 offset:59392
	v_pk_fma_f32 v[192:193], v[64:65], v[226:227], v[192:193]
	s_waitcnt lgkmcnt(11)
	v_pk_fma_f32 v[192:193], v[78:79], v[228:229], v[192:193]
	ds_read_b128 v[224:227], v105 offset:60416
	v_pk_fma_f32 v[192:193], v[66:67], v[230:231], v[192:193]
	v_add_f32_e32 v1, v192, v193
	v_mov_b32_e32 v25, 0
	s_nop 0
	s_nop 0
	v_add_f32_dpp v1, v1, v1 row_shr:1 row_mask:0xf bank_mask:0xf bound_ctrl:1
	s_nop 1
	v_add_f32_dpp v1, v1, v1 row_shr:2 row_mask:0xf bank_mask:0xf bound_ctrl:1
	s_nop 1
	v_add_f32_dpp v1, v1, v1 row_shr:4 row_mask:0xf bank_mask:0xf bound_ctrl:1
	s_nop 1
	v_add_f32_dpp v1, v1, v1 row_shr:8 row_mask:0xf bank_mask:0xf bound_ctrl:1
	s_nop 1
	v_mov_b32_dpp v25, v1 row_bcast:15 row_mask:0xa bank_mask:0xf
	v_add_f32_e32 v1, v1, v25
	v_mov_b32_e32 v25, 0
	s_nop 1
	v_mov_b32_dpp v25, v1 row_bcast:31 row_mask:0xc bank_mask:0xf
	v_add_f32_e32 v1, v1, v25
	s_nop 0
	s_waitcnt lgkmcnt(11)
	v_pk_mul_f32 v[190:191], v[84:85], v[232:233]
	ds_read_b128 v[228:231], v105 offset:61440
	v_pk_fma_f32 v[190:191], v[72:73], v[234:235], v[190:191]
	v_readlane_b32 s66, v1, 63
	s_nop 0
	s_nop 0
	s_waitcnt lgkmcnt(11)
	v_pk_fma_f32 v[190:191], v[88:89], v[240:241], v[190:191]
	ds_read_b128 v[232:235], v105 offset:62464
	v_pk_fma_f32 v[190:191], v[62:63], v[242:243], v[190:191]
	s_waitcnt lgkmcnt(11)
	v_pk_fma_f32 v[190:191], v[80:81], v[244:245], v[190:191]
	ds_read_b128 v[240:243], v105 offset:63488
	v_pk_fma_f32 v[190:191], v[70:71], v[246:247], v[190:191]
	s_waitcnt lgkmcnt(11)
	v_pk_fma_f32 v[190:191], v[86:87], v[248:249], v[190:191]
	ds_read_b128 v[244:247], v105 offset:64512
	v_pk_fma_f32 v[190:191], v[60:61], v[250:251], v[190:191]
	s_waitcnt lgkmcnt(11)
	v_pk_fma_f32 v[190:191], v[76:77], v[196:197], v[190:191]
	v_pk_fma_f32 v[190:191], v[68:69], v[198:199], v[190:191]
	s_waitcnt lgkmcnt(10)
	v_pk_fma_f32 v[190:191], v[82:83], v[200:201], v[190:191]
	v_pk_fma_f32 v[190:191], v[58:59], v[202:203], v[190:191]
	s_waitcnt lgkmcnt(9)
	v_pk_fma_f32 v[190:191], v[74:75], v[204:205], v[190:191]
	v_pk_fma_f32 v[190:191], v[64:65], v[206:207], v[190:191]
	s_nop 0
	s_waitcnt lgkmcnt(8)
	v_pk_fma_f32 v[190:191], v[78:79], v[208:209], v[190:191]
	v_pk_fma_f32 v[190:191], v[66:67], v[210:211], v[190:191]
	v_add_f32_e32 v1, v190, v191
	v_mov_b32_e32 v25, 0
	s_nop 0
	s_nop 0
	v_add_f32_dpp v1, v1, v1 row_shr:1 row_mask:0xf bank_mask:0xf bound_ctrl:1
	s_nop 0
	s_waitcnt lgkmcnt(6)
	v_pk_mul_f32 v[192:193], v[88:89], v[216:217]
	v_pk_fma_f32 v[192:193], v[62:63], v[218:219], v[192:193]
	v_add_f32_dpp v1, v1, v1 row_shr:2 row_mask:0xf bank_mask:0xf bound_ctrl:1
	s_nop 0
	s_nop 0
	v_add_f32_dpp v1, v1, v1 row_shr:4 row_mask:0xf bank_mask:0xf bound_ctrl:1
	s_nop 1
	v_add_f32_dpp v1, v1, v1 row_shr:8 row_mask:0xf bank_mask:0xf bound_ctrl:1
	s_nop 1
	v_mov_b32_dpp v25, v1 row_bcast:15 row_mask:0xa bank_mask:0xf
	v_add_f32_e32 v1, v1, v25
	v_mov_b32_e32 v25, 0
	s_nop 1
	v_mov_b32_dpp v25, v1 row_bcast:31 row_mask:0xc bank_mask:0xf
	v_add_f32_e32 v1, v1, v25
	v_pk_fma_f32 v[192:193], v[84:85], v[212:213], v[192:193]
	v_pk_fma_f32 v[192:193], v[72:73], v[214:215], v[192:193]
	v_readlane_b32 s67, v1, 63
	s_nop 0
	s_nop 0
	s_nop 0
	s_waitcnt lgkmcnt(5)
	v_pk_fma_f32 v[192:193], v[80:81], v[220:221], v[192:193]
	v_pk_fma_f32 v[192:193], v[70:71], v[222:223], v[192:193]
	s_waitcnt lgkmcnt(4)
	v_pk_fma_f32 v[192:193], v[86:87], v[224:225], v[192:193]
	v_pk_fma_f32 v[192:193], v[60:61], v[226:227], v[192:193]
	s_waitcnt lgkmcnt(3)
	v_pk_fma_f32 v[192:193], v[76:77], v[228:229], v[192:193]
	v_pk_fma_f32 v[192:193], v[68:69], v[230:231], v[192:193]
	s_waitcnt lgkmcnt(2)
	v_pk_fma_f32 v[192:193], v[82:83], v[232:233], v[192:193]
	v_pk_fma_f32 v[192:193], v[58:59], v[234:235], v[192:193]
	s_waitcnt lgkmcnt(1)
	v_pk_fma_f32 v[192:193], v[74:75], v[240:241], v[192:193]
	v_pk_fma_f32 v[192:193], v[64:65], v[242:243], v[192:193]
	s_waitcnt lgkmcnt(0)
	v_pk_fma_f32 v[192:193], v[78:79], v[244:245], v[192:193]
	v_pk_fma_f32 v[192:193], v[66:67], v[246:247], v[192:193]
	v_add_f32_e32 v1, v192, v193
	v_mov_b32_e32 v25, 0
	s_nop 0
	v_add_f32_dpp v1, v1, v1 row_shr:1 row_mask:0xf bank_mask:0xf bound_ctrl:1
	s_nop 1
	v_add_f32_dpp v1, v1, v1 row_shr:2 row_mask:0xf bank_mask:0xf bound_ctrl:1
	s_nop 1
	v_add_f32_dpp v1, v1, v1 row_shr:4 row_mask:0xf bank_mask:0xf bound_ctrl:1
	s_nop 1
	v_add_f32_dpp v1, v1, v1 row_shr:8 row_mask:0xf bank_mask:0xf bound_ctrl:1
	s_nop 1
	v_mov_b32_dpp v25, v1 row_bcast:15 row_mask:0xa bank_mask:0xf
	v_add_f32_e32 v1, v1, v25
	v_mov_b32_e32 v25, 0
	s_nop 1
	v_mov_b32_dpp v25, v1 row_bcast:31 row_mask:0xc bank_mask:0xf
	v_add_f32_e32 v1, v1, v25
	s_nop 0
	v_readlane_b32 s68, v1, 63
	s_and_saveexec_b64 s[26:27], s[8:9]
	s_cbranch_execz .LBB0_1306
	v_mov_b32_e32 v1, s34
	v_cndmask_b32_e64 v1, 0, v1, s[6:7]
	v_mov_b32_e32 v25, s38
	v_cndmask_b32_e64 v1, v1, v25, s[22:23]
	v_mov_b32_e32 v25, s39
	v_cndmask_b32_e64 v1, v1, v25, s[20:21]
	v_mov_b32_e32 v25, s62
	v_cndmask_b32_e64 v1, v1, v25, s[18:19]
	v_mov_b32_e32 v25, s63
	v_cndmask_b32_e64 v1, v1, v25, s[16:17]
	v_mov_b32_e32 v25, s66
	v_cndmask_b32_e64 v1, v1, v25, s[14:15]
	v_mov_b32_e32 v25, s67
	v_cndmask_b32_e64 v1, v1, v25, s[12:13]
	v_mov_b32_e32 v25, s68
	v_cndmask_b32_e64 v1, v1, v25, s[10:11]
	global_load_dword v25, v[18:19], off
	s_mov_b32 s34, 0x3f200000
	s_waitcnt vmcnt(0) lgkmcnt(0)
	v_add_f32_e32 v1, v1, v25
	v_mul_f32_e32 v1, 0x3d888889, v1
	v_cmp_nlt_f32_e64 s[38:39], |v1|, s34
	s_and_saveexec_b64 s[62:63], s[38:39]
	s_xor_b64 s[38:39], exec, s[62:63]
	s_cbranch_execz .LBB0_1314
	v_add_f32_e64 v25, |v1|, |v1|
	v_mul_f32_e32 v58, 0x3fb8aa3b, v25
	v_rndne_f32_e32 v59, v58
	s_mov_b32 s34, 0x3fb8aa3b
	v_sub_f32_e32 v60, v58, v59
	v_fma_f32 v58, v25, s34, -v58
	v_fmac_f32_e32 v58, 0x32a5705f, v25
	v_add_f32_e32 v58, v60, v58
	v_cvt_i32_f32_e32 v59, v59
	v_exp_f32_e32 v58, v58
	s_mov_b32 s34, 0xc2ce8ed0
	v_cmp_ngt_f32_e32 vcc, s34, v25
	v_ldexp_f32 v58, v58, v59
	s_nop 0
	v_cndmask_b32_e32 v58, 0, v58, vcc
	v_cmp_nlt_f32_e32 vcc, s44, v25
	s_nop 1
	v_cndmask_b32_e32 v25, v111, v58, vcc
	v_add_f32_e32 v25, 1.0, v25
	v_rcp_f32_e32 v25, v25
	s_nop 0
	v_fma_f32 v25, v25, -2.0, 1.0

; #define LAS __attribute__((address_space(3)))
; __device__ __forceinline__ float wave_max(float v) { return lane63(scan64<true>(v)); }
; template <int YMODE, int EXTRA, bool NORM_OUT, bool XN8  , bool XIN_BF = false  , bool XOUT_BF = false  > ...
;     ...
;                     for (int j = 0; j < 8; ++j) am = fmaxf(fmaxf(am, fmaxf(fabsf(x[j][0]), fabsf(x[j][1]))), fmaxf(fabsf(x[j][2]), fabsf(x[j][3])));
;                     am = wave_max(am);
;                     const float inv = am > 0.f ? 127.f / am : 0.f;
;                     if (F.lane == 0) { rowmax[row] = am; if (EXTRA == 2) route[384 + rl] = am; }
; #pragma unroll
;                     for (int j = 0; j < 8; ++j) *(unsigned*)((unsigned char*)XN + row * D + 256 * j + 4 * F.lane) = pack_i8x4(x[j][0] * inv, x[j][1] * inv, x[j][2] * inv, x[j][3] * inv);
;     ...
;                     for (int e = 0; e < 8; ++e) { float s = 0.f;
; #pragma unroll
;                         for (int j = 0; j < 8; ++j) { const f32x4 w = *(const LAS f32x4*)(we + e * D + 256 * j + 4 * F.lane); s += (x[j][0] * w[0] + x[j][1] * w[1]) + (x[j][2] * w[2] + x[j][3] * w[3]); }
.LBB0_2181:
	s_or_b64 exec, exec, s[12:13]
	ds_read_b128 v[196:199], v118
	ds_read_b128 v[200:203], v118 offset:1024
	ds_read_b128 v[204:207], v118 offset:2048
	ds_read_b128 v[208:211], v118 offset:3072
	ds_read_b128 v[212:215], v118 offset:4096
	ds_read_b128 v[216:219], v118 offset:5120
	ds_read_b128 v[220:223], v118 offset:6144
	ds_read_b128 v[224:227], v118 offset:7168
	ds_read_b128 v[228:231], v118 offset:8192
	ds_read_b128 v[232:235], v118 offset:9216
	ds_read_b128 v[240:243], v118 offset:10240
	ds_read_b128 v[244:247], v118 offset:11264
	v_div_scale_f32 v2, s[16:17], s14, s14, v125
	v_rcp_f32_e32 v88, v2
	s_mov_b32 s15, 0x42fe0000
	v_cmp_gt_f32_e64 s[12:13], s14, 0
	s_lshl_b64 s[0:1], s[0:1], 11
	v_fma_f32 v89, -v2, v88, 1.0
	v_fmac_f32_e32 v88, v89, v88
	v_mov_b32_e32 v89, s14
	v_div_scale_f32 v89, vcc, s15, v89, s15
	v_mul_f32_e32 v90, v89, v88
	v_fma_f32 v91, -v2, v90, v89
	v_fmac_f32_e32 v90, v91, v88
	v_fma_f32 v2, -v2, v90, v89
	v_div_fmas_f32 v2, v2, v88, v90
	v_div_fixup_f32 v2, v2, s14, v125
	v_cndmask_b32_e64 v2, 0, v2, s[12:13]
	v_mul_f32_e32 v89, v87, v2
	v_mul_f32_e32 v88, v86, v2
	v_mul_f32_e32 v90, v84, v2
	v_mul_f32_e32 v91, v85, v2
	v_med3_f32 v89, v89, s46, v125
	v_med3_f32 v88, v88, s46, v125
	v_rndne_f32_e32 v89, v89
	v_med3_f32 v90, v90, s46, v125
	v_med3_f32 v91, v91, s46, v125
	v_rndne_f32_e32 v88, v88
	v_cvt_i32_f32_e32 v89, v89
	v_rndne_f32_e32 v90, v90
	v_rndne_f32_e32 v91, v91
	v_cvt_i32_f32_e32 v88, v88
	v_cvt_i32_f32_sdwa v90, v90 dst_sel:WORD_1 dst_unused:UNUSED_PAD src0_sel:DWORD
	v_cvt_i32_f32_e32 v91, v91
	v_lshlrev_b32_e32 v89, 8, v89
	v_and_b32_e32 v89, 0xff00, v89
	v_and_b32_e32 v90, 0xff0000, v90
	v_perm_b32 v88, v91, v88, s47
	v_or3_b32 v90, v88, v89, v90
	v_lshl_add_u64 v[88:89], v[22:23], 0, s[0:1]
	v_mul_f32_e32 v91, v83, v2
	global_store_dword v[88:89], v90, off
	v_mul_f32_e32 v90, v82, v2
	v_mul_f32_e32 v92, v80, v2
	v_mul_f32_e32 v93, v81, v2
	v_med3_f32 v91, v91, s46, v125
	v_med3_f32 v90, v90, s46, v125
	v_rndne_f32_e32 v91, v91
	v_med3_f32 v92, v92, s46, v125
	v_med3_f32 v93, v93, s46, v125
	v_rndne_f32_e32 v90, v90
	v_cvt_i32_f32_e32 v91, v91
	v_rndne_f32_e32 v92, v92
	v_rndne_f32_e32 v93, v93
	v_cvt_i32_f32_e32 v90, v90
	v_cvt_i32_f32_sdwa v92, v92 dst_sel:WORD_1 dst_unused:UNUSED_PAD src0_sel:DWORD
	v_cvt_i32_f32_e32 v93, v93
	v_lshlrev_b32_e32 v91, 8, v91
	v_and_b32_e32 v91, 0xff00, v91
	v_and_b32_e32 v92, 0xff0000, v92
	v_perm_b32 v90, v93, v90, s47
	v_or3_b32 v90, v90, v91, v92
	v_mul_f32_e32 v91, v79, v2
	global_store_dword v[88:89], v90, off offset:256
	v_mul_f32_e32 v90, v78, v2
	v_mul_f32_e32 v92, v76, v2
	v_mul_f32_e32 v93, v77, v2
	v_med3_f32 v91, v91, s46, v125
	v_med3_f32 v90, v90, s46, v125
	v_rndne_f32_e32 v91, v91
	v_med3_f32 v92, v92, s46, v125
	v_med3_f32 v93, v93, s46, v125
	v_rndne_f32_e32 v90, v90
	v_cvt_i32_f32_e32 v91, v91
	v_rndne_f32_e32 v92, v92
	v_rndne_f32_e32 v93, v93
	v_cvt_i32_f32_e32 v90, v90
	v_cvt_i32_f32_sdwa v92, v92 dst_sel:WORD_1 dst_unused:UNUSED_PAD src0_sel:DWORD
	v_cvt_i32_f32_e32 v93, v93
	v_lshlrev_b32_e32 v91, 8, v91
	v_and_b32_e32 v91, 0xff00, v91
	v_and_b32_e32 v92, 0xff0000, v92
	v_perm_b32 v90, v93, v90, s47
	v_or3_b32 v90, v90, v91, v92
	v_mul_f32_e32 v91, v75, v2
	global_store_dword v[88:89], v90, off offset:512
	v_mul_f32_e32 v90, v74, v2
	v_mul_f32_e32 v92, v72, v2
	v_mul_f32_e32 v93, v73, v2
	v_med3_f32 v91, v91, s46, v125
	v_med3_f32 v90, v90, s46, v125
	v_rndne_f32_e32 v91, v91
	v_med3_f32 v92, v92, s46, v125
	v_med3_f32 v93, v93, s46, v125
	v_rndne_f32_e32 v90, v90
	v_cvt_i32_f32_e32 v91, v91
	v_rndne_f32_e32 v92, v92
	v_rndne_f32_e32 v93, v93
	v_cvt_i32_f32_e32 v90, v90
	v_cvt_i32_f32_sdwa v92, v92 dst_sel:WORD_1 dst_unused:UNUSED_PAD src0_sel:DWORD
	v_cvt_i32_f32_e32 v93, v93
	v_lshlrev_b32_e32 v91, 8, v91
	v_and_b32_e32 v91, 0xff00, v91
	v_and_b32_e32 v92, 0xff0000, v92
	v_perm_b32 v90, v93, v90, s47
	v_or3_b32 v90, v90, v91, v92
	v_mul_f32_e32 v91, v71, v2
	global_store_dword v[88:89], v90, off offset:768
	v_mul_f32_e32 v90, v70, v2
	v_mul_f32_e32 v92, v68, v2
	v_mul_f32_e32 v93, v69, v2
	v_med3_f32 v91, v91, s46, v125
	v_med3_f32 v90, v90, s46, v125
	v_rndne_f32_e32 v91, v91
	v_med3_f32 v92, v92, s46, v125
	v_med3_f32 v93, v93, s46, v125
	v_rndne_f32_e32 v90, v90
	v_cvt_i32_f32_e32 v91, v91
	v_rndne_f32_e32 v92, v92
	v_rndne_f32_e32 v93, v93
	v_cvt_i32_f32_e32 v90, v90
	v_cvt_i32_f32_sdwa v92, v92 dst_sel:WORD_1 dst_unused:UNUSED_PAD src0_sel:DWORD
	v_cvt_i32_f32_e32 v93, v93
	v_lshlrev_b32_e32 v91, 8, v91
	v_and_b32_e32 v91, 0xff00, v91
	v_and_b32_e32 v92, 0xff0000, v92
	v_perm_b32 v90, v93, v90, s47
	v_or3_b32 v90, v90, v91, v92
	v_mul_f32_e32 v91, v67, v2
	global_store_dword v[88:89], v90, off offset:1024
	v_mul_f32_e32 v90, v66, v2
	v_mul_f32_e32 v92, v64, v2
	v_mul_f32_e32 v93, v65, v2
	v_med3_f32 v91, v91, s46, v125
	v_med3_f32 v90, v90, s46, v125
	v_rndne_f32_e32 v91, v91
	v_med3_f32 v92, v92, s46, v125
	v_med3_f32 v93, v93, s46, v125
	v_rndne_f32_e32 v90, v90
	v_cvt_i32_f32_e32 v91, v91
	v_rndne_f32_e32 v92, v92
	v_rndne_f32_e32 v93, v93
	v_cvt_i32_f32_e32 v90, v90
	v_cvt_i32_f32_sdwa v92, v92 dst_sel:WORD_1 dst_unused:UNUSED_PAD src0_sel:DWORD
	v_cvt_i32_f32_e32 v93, v93
	v_lshlrev_b32_e32 v91, 8, v91
	v_and_b32_e32 v91, 0xff00, v91
	v_and_b32_e32 v92, 0xff0000, v92
	v_perm_b32 v90, v93, v90, s47
	v_or3_b32 v90, v90, v91, v92
	v_mul_f32_e32 v91, v63, v2
	global_store_dword v[88:89], v90, off offset:1280
	v_mul_f32_e32 v90, v62, v2
	v_mul_f32_e32 v92, v60, v2
	v_mul_f32_e32 v93, v61, v2
	v_med3_f32 v91, v91, s46, v125
	v_med3_f32 v90, v90, s46, v125
	v_rndne_f32_e32 v91, v91
	v_med3_f32 v92, v92, s46, v125
	v_med3_f32 v93, v93, s46, v125
	v_rndne_f32_e32 v90, v90
	v_cvt_i32_f32_e32 v91, v91
	v_rndne_f32_e32 v92, v92
	v_rndne_f32_e32 v93, v93
	v_cvt_i32_f32_e32 v90, v90
	v_cvt_i32_f32_sdwa v92, v92 dst_sel:WORD_1 dst_unused:UNUSED_PAD src0_sel:DWORD
	v_cvt_i32_f32_e32 v93, v93
	v_lshlrev_b32_e32 v91, 8, v91
	v_and_b32_e32 v91, 0xff00, v91
	v_and_b32_e32 v92, 0xff0000, v92
	v_perm_b32 v90, v93, v90, s47
	v_or3_b32 v90, v90, v91, v92
	v_mul_f32_e32 v91, v59, v2
	global_store_dword v[88:89], v90, off offset:1536
	v_mul_f32_e32 v90, v58, v2
	v_mul_f32_e32 v92, v56, v2
	v_mul_f32_e32 v2, v57, v2
	v_med3_f32 v91, v91, s46, v125
	v_med3_f32 v90, v90, s46, v125
	v_rndne_f32_e32 v91, v91
	v_med3_f32 v92, v92, s46, v125
	v_med3_f32 v2, v2, s46, v125
	v_rndne_f32_e32 v90, v90
	v_cvt_i32_f32_e32 v91, v91
	v_rndne_f32_e32 v92, v92
	v_rndne_f32_e32 v2, v2
	v_cvt_i32_f32_e32 v90, v90
	v_cvt_i32_f32_sdwa v92, v92 dst_sel:WORD_1 dst_unused:UNUSED_PAD src0_sel:DWORD
	v_cvt_i32_f32_e32 v2, v2
	v_lshlrev_b32_e32 v91, 8, v91
	v_and_b32_e32 v91, 0xff00, v91
	v_and_b32_e32 v92, 0xff0000, v92
	v_perm_b32 v2, v2, v90, s47
	v_or3_b32 v2, v2, v91, v92
	global_store_dword v[88:89], v2, off offset:1792
	s_nop 0
	s_waitcnt lgkmcnt(12)
; #define LAS __attribute__((address_space(3)))
; __device__ __forceinline__ float wave_sum(float v) { return lane63(scan64<false>(v)); }
; template <int YMODE, int EXTRA, bool NORM_OUT, bool XN8  , bool XIN_BF = false  , bool XOUT_BF = false  > ...
;     ...
;                     float d8[8];
; #pragma unroll
;                     for (int e = 0; e < 8; ++e) { float s = 0.f;
; #pragma unroll
;                         for (int j = 0; j < 8; ++j) { const f32x4 w = *(const LAS f32x4*)(we + e * D + 256 * j + 4 * F.lane); s += (x[j][0] * w[0] + x[j][1] * w[1]) + (x[j][2] * w[2] + x[j][3] * w[3]); }
;                         d8[e] = wave_sum(s); asm volatile("" ::: "memory"); }
	s_waitcnt lgkmcnt(11)
	v_pk_mul_f32 v[190:191], v[86:87], v[196:197]
	ds_read_b128 v[248:251], v118 offset:12288
	v_pk_fma_f32 v[190:191], v[84:85], v[198:199], v[190:191]
	s_waitcnt lgkmcnt(11)
	v_pk_fma_f32 v[190:191], v[82:83], v[200:201], v[190:191]
	ds_read_b128 v[196:199], v118 offset:13312
	v_pk_fma_f32 v[190:191], v[80:81], v[202:203], v[190:191]
	s_waitcnt lgkmcnt(11)
	v_pk_fma_f32 v[190:191], v[78:79], v[204:205], v[190:191]
	ds_read_b128 v[200:203], v118 offset:14336
	v_pk_fma_f32 v[190:191], v[76:77], v[206:207], v[190:191]
	s_waitcnt lgkmcnt(11)
	v_pk_fma_f32 v[190:191], v[74:75], v[208:209], v[190:191]
	ds_read_b128 v[204:207], v118 offset:15360
	v_pk_fma_f32 v[190:191], v[72:73], v[210:211], v[190:191]
	s_waitcnt lgkmcnt(11)
	v_pk_fma_f32 v[190:191], v[70:71], v[212:213], v[190:191]
	ds_read_b128 v[208:211], v118 offset:16384
	v_pk_fma_f32 v[190:191], v[68:69], v[214:215], v[190:191]
	s_waitcnt lgkmcnt(11)
	v_pk_fma_f32 v[190:191], v[66:67], v[216:217], v[190:191]
	ds_read_b128 v[212:215], v118 offset:17408
	v_pk_fma_f32 v[190:191], v[64:65], v[218:219], v[190:191]
	s_waitcnt lgkmcnt(11)
	v_pk_fma_f32 v[190:191], v[62:63], v[220:221], v[190:191]
	ds_read_b128 v[216:219], v118 offset:18432
	v_pk_fma_f32 v[190:191], v[60:61], v[222:223], v[190:191]
	s_waitcnt lgkmcnt(11)
	v_pk_fma_f32 v[190:191], v[58:59], v[224:225], v[190:191]
	ds_read_b128 v[220:223], v118 offset:19456
	v_pk_fma_f32 v[190:191], v[56:57], v[226:227], v[190:191]
	v_add_f32_e32 v2, v190, v191
	v_mov_b32_e32 v88, 0
	s_nop 0
	v_add_f32_dpp v2, v2, v2 row_shr:1 row_mask:0xf bank_mask:0xf bound_ctrl:1
	s_nop 1
	v_add_f32_dpp v2, v2, v2 row_shr:2 row_mask:0xf bank_mask:0xf bound_ctrl:1
	s_nop 1
	v_add_f32_dpp v2, v2, v2 row_shr:4 row_mask:0xf bank_mask:0xf bound_ctrl:1
	s_nop 1
	v_add_f32_dpp v2, v2, v2 row_shr:8 row_mask:0xf bank_mask:0xf bound_ctrl:1
	s_nop 1
	v_mov_b32_dpp v88, v2 row_bcast:15 row_mask:0xa bank_mask:0xf
	v_add_f32_e32 v2, v2, v88
	v_mov_b32_e32 v88, 0
	s_nop 1
	v_mov_b32_dpp v88, v2 row_bcast:31 row_mask:0xc bank_mask:0xf
	v_add_f32_e32 v2, v2, v88
	s_nop 0
	v_readlane_b32 s24, v2, 63
	s_nop 0
	s_waitcnt lgkmcnt(11)
	v_pk_mul_f32 v[192:193], v[86:87], v[228:229]
	ds_read_b128 v[224:227], v118 offset:20480
	v_pk_fma_f32 v[192:193], v[84:85], v[230:231], v[192:193]
	s_waitcnt lgkmcnt(11)
	v_pk_fma_f32 v[192:193], v[82:83], v[232:233], v[192:193]
	ds_read_b128 v[228:231], v118 offset:21504
	v_pk_fma_f32 v[192:193], v[80:81], v[234:235], v[192:193]
	s_waitcnt lgkmcnt(11)
	v_pk_fma_f32 v[192:193], v[78:79], v[240:241], v[192:193]
	ds_read_b128 v[232:235], v118 offset:22528
	v_pk_fma_f32 v[192:193], v[76:77], v[242:243], v[192:193]
	s_waitcnt lgkmcnt(11)
	v_pk_fma_f32 v[192:193], v[74:75], v[244:245], v[192:193]
	ds_read_b128 v[240:243], v118 offset:23552
	v_pk_fma_f32 v[192:193], v[72:73], v[246:247], v[192:193]
	s_waitcnt lgkmcnt(11)
	v_pk_fma_f32 v[192:193], v[70:71], v[248:249], v[192:193]
	ds_read_b128 v[244:247], v118 offset:24576
	v_pk_fma_f32 v[192:193], v[68:69], v[250:251], v[192:193]
	s_waitcnt lgkmcnt(11)
	v_pk_fma_f32 v[192:193], v[66:67], v[196:197], v[192:193]
	ds_read_b128 v[248:251], v118 offset:25600
	v_pk_fma_f32 v[192:193], v[64:65], v[198:199], v[192:193]
	s_waitcnt lgkmcnt(11)
	v_pk_fma_f32 v[192:193], v[62:63], v[200:201], v[192:193]
	ds_read_b128 v[196:199], v118 offset:26624
	v_pk_fma_f32 v[192:193], v[60:61], v[202:203], v[192:193]
	s_waitcnt lgkmcnt(11)
	v_pk_fma_f32 v[192:193], v[58:59], v[204:205], v[192:193]
	ds_read_b128 v[200:203], v118 offset:27648
	v_pk_fma_f32 v[192:193], v[56:57], v[206:207], v[192:193]
	v_add_f32_e32 v2, v192, v193
	v_mov_b32_e32 v88, 0
	s_nop 0
	v_add_f32_dpp v2, v2, v2 row_shr:1 row_mask:0xf bank_mask:0xf bound_ctrl:1
	s_nop 1
	v_add_f32_dpp v2, v2, v2 row_shr:2 row_mask:0xf bank_mask:0xf bound_ctrl:1
	s_nop 1
	v_add_f32_dpp v2, v2, v2 row_shr:4 row_mask:0xf bank_mask:0xf bound_ctrl:1
	s_nop 1
	v_add_f32_dpp v2, v2, v2 row_shr:8 row_mask:0xf bank_mask:0xf bound_ctrl:1
	s_nop 1
	v_mov_b32_dpp v88, v2 row_bcast:15 row_mask:0xa bank_mask:0xf
	v_add_f32_e32 v2, v2, v88
	v_mov_b32_e32 v88, 0
	s_nop 1
	v_mov_b32_dpp v88, v2 row_bcast:31 row_mask:0xc bank_mask:0xf
	v_add_f32_e32 v2, v2, v88
	s_nop 0
	v_readlane_b32 s25, v2, 63
	s_nop 0
	s_waitcnt lgkmcnt(11)
	v_pk_mul_f32 v[190:191], v[86:87], v[208:209]
	ds_read_b128 v[204:207], v118 offset:28672
	v_pk_fma_f32 v[190:191], v[84:85], v[210:211], v[190:191]
	s_waitcnt lgkmcnt(11)
	v_pk_fma_f32 v[190:191], v[82:83], v[212:213], v[190:191]
	ds_read_b128 v[208:211], v118 offset:29696
	v_pk_fma_f32 v[190:191], v[80:81], v[214:215], v[190:191]
	s_waitcnt lgkmcnt(11)
	v_pk_fma_f32 v[190:191], v[78:79], v[216:217], v[190:191]
	ds_read_b128 v[212:215], v118 offset:30720
	v_pk_fma_f32 v[190:191], v[76:77], v[218:219], v[190:191]
	s_waitcnt lgkmcnt(11)
	v_pk_fma_f32 v[190:191], v[74:75], v[220:221], v[190:191]
	ds_read_b128 v[216:219], v118 offset:31744
	v_pk_fma_f32 v[190:191], v[72:73], v[222:223], v[190:191]
	s_waitcnt lgkmcnt(11)
	v_pk_fma_f32 v[190:191], v[70:71], v[224:225], v[190:191]
	ds_read_b128 v[220:223], v118 offset:32768
	v_pk_fma_f32 v[190:191], v[68:69], v[226:227], v[190:191]
	s_waitcnt lgkmcnt(11)
	v_pk_fma_f32 v[190:191], v[66:67], v[228:229], v[190:191]
	ds_read_b128 v[224:227], v118 offset:33792
	v_pk_fma_f32 v[190:191], v[64:65], v[230:231], v[190:191]
	s_waitcnt lgkmcnt(11)
	v_pk_fma_f32 v[190:191], v[62:63], v[232:233], v[190:191]
	ds_read_b128 v[228:231], v118 offset:34816
	v_pk_fma_f32 v[190:191], v[60:61], v[234:235], v[190:191]
	s_waitcnt lgkmcnt(11)
; #define LAS __attribute__((address_space(3)))
; __device__ __forceinline__ float wave_sum(float v) { return lane63(scan64<false>(v)); }
; template <int YMODE, int EXTRA, bool NORM_OUT, bool XN8  , bool XIN_BF = false  , bool XOUT_BF = false  > ...
;     ...
;                     float d8[8];
; #pragma unroll
;                     for (int e = 0; e < 8; ++e) { float s = 0.f;
; #pragma unroll
;                         for (int j = 0; j < 8; ++j) { const f32x4 w = *(const LAS f32x4*)(we + e * D + 256 * j + 4 * F.lane); s += (x[j][0] * w[0] + x[j][1] * w[1]) + (x[j][2] * w[2] + x[j][3] * w[3]); }
;                         d8[e] = wave_sum(s); asm volatile("" ::: "memory"); }
	v_pk_fma_f32 v[190:191], v[58:59], v[240:241], v[190:191]
	ds_read_b128 v[232:235], v118 offset:35840
	v_pk_fma_f32 v[190:191], v[56:57], v[242:243], v[190:191]
	v_add_f32_e32 v2, v190, v191
	v_mov_b32_e32 v88, 0
	s_nop 0
	v_add_f32_dpp v2, v2, v2 row_shr:1 row_mask:0xf bank_mask:0xf bound_ctrl:1
	s_nop 1
	v_add_f32_dpp v2, v2, v2 row_shr:2 row_mask:0xf bank_mask:0xf bound_ctrl:1
	s_nop 1
	v_add_f32_dpp v2, v2, v2 row_shr:4 row_mask:0xf bank_mask:0xf bound_ctrl:1
	s_nop 1
	v_add_f32_dpp v2, v2, v2 row_shr:8 row_mask:0xf bank_mask:0xf bound_ctrl:1
	s_nop 1
	v_mov_b32_dpp v88, v2 row_bcast:15 row_mask:0xa bank_mask:0xf
	v_add_f32_e32 v2, v2, v88
	v_mov_b32_e32 v88, 0
	s_nop 1
	v_mov_b32_dpp v88, v2 row_bcast:31 row_mask:0xc bank_mask:0xf
	v_add_f32_e32 v2, v2, v88
	s_nop 0
	v_readlane_b32 s26, v2, 63
	s_nop 0
	s_waitcnt lgkmcnt(11)
	v_pk_mul_f32 v[192:193], v[86:87], v[244:245]
	ds_read_b128 v[240:243], v118 offset:36864
	v_pk_fma_f32 v[192:193], v[84:85], v[246:247], v[192:193]
	s_waitcnt lgkmcnt(11)
	v_pk_fma_f32 v[192:193], v[82:83], v[248:249], v[192:193]
	ds_read_b128 v[244:247], v118 offset:37888
	v_pk_fma_f32 v[192:193], v[80:81], v[250:251], v[192:193]
	s_waitcnt lgkmcnt(11)
	v_pk_fma_f32 v[192:193], v[78:79], v[196:197], v[192:193]
	ds_read_b128 v[248:251], v118 offset:38912
	v_pk_fma_f32 v[192:193], v[76:77], v[198:199], v[192:193]
	s_waitcnt lgkmcnt(11)
	v_pk_fma_f32 v[192:193], v[74:75], v[200:201], v[192:193]
	ds_read_b128 v[196:199], v118 offset:39936
	v_pk_fma_f32 v[192:193], v[72:73], v[202:203], v[192:193]
	s_waitcnt lgkmcnt(11)
	v_pk_fma_f32 v[192:193], v[70:71], v[204:205], v[192:193]
	ds_read_b128 v[200:203], v118 offset:40960
	v_pk_fma_f32 v[192:193], v[68:69], v[206:207], v[192:193]
	s_waitcnt lgkmcnt(11)
	v_pk_fma_f32 v[192:193], v[66:67], v[208:209], v[192:193]
	ds_read_b128 v[204:207], v118 offset:41984
	v_pk_fma_f32 v[192:193], v[64:65], v[210:211], v[192:193]
	s_waitcnt lgkmcnt(11)
	v_pk_fma_f32 v[192:193], v[62:63], v[212:213], v[192:193]
	ds_read_b128 v[208:211], v118 offset:43008
	v_pk_fma_f32 v[192:193], v[60:61], v[214:215], v[192:193]
	s_waitcnt lgkmcnt(11)
	v_pk_fma_f32 v[192:193], v[58:59], v[216:217], v[192:193]
	ds_read_b128 v[212:215], v118 offset:44032
	v_pk_fma_f32 v[192:193], v[56:57], v[218:219], v[192:193]
	v_add_f32_e32 v2, v192, v193
	v_mov_b32_e32 v88, 0
	s_nop 0
	v_add_f32_dpp v2, v2, v2 row_shr:1 row_mask:0xf bank_mask:0xf bound_ctrl:1
	s_nop 1
	v_add_f32_dpp v2, v2, v2 row_shr:2 row_mask:0xf bank_mask:0xf bound_ctrl:1
	s_nop 1
	v_add_f32_dpp v2, v2, v2 row_shr:4 row_mask:0xf bank_mask:0xf bound_ctrl:1
	s_nop 1
	v_add_f32_dpp v2, v2, v2 row_shr:8 row_mask:0xf bank_mask:0xf bound_ctrl:1
	s_nop 1
	v_mov_b32_dpp v88, v2 row_bcast:15 row_mask:0xa bank_mask:0xf
	v_add_f32_e32 v2, v2, v88
	v_mov_b32_e32 v88, 0
	s_nop 1
	v_mov_b32_dpp v88, v2 row_bcast:31 row_mask:0xc bank_mask:0xf
	v_add_f32_e32 v2, v2, v88
	s_nop 0
	v_readlane_b32 s27, v2, 63
	s_nop 0
	s_waitcnt lgkmcnt(11)
	v_pk_mul_f32 v[190:191], v[86:87], v[220:221]
	ds_read_b128 v[216:219], v118 offset:45056
	v_pk_fma_f32 v[190:191], v[84:85], v[222:223], v[190:191]
	s_waitcnt lgkmcnt(11)
	v_pk_fma_f32 v[190:191], v[82:83], v[224:225], v[190:191]
	ds_read_b128 v[220:223], v118 offset:46080
	v_pk_fma_f32 v[190:191], v[80:81], v[226:227], v[190:191]
	s_waitcnt lgkmcnt(11)
	v_pk_fma_f32 v[190:191], v[78:79], v[228:229], v[190:191]
	ds_read_b128 v[224:227], v118 offset:47104
	v_pk_fma_f32 v[190:191], v[76:77], v[230:231], v[190:191]
	s_waitcnt lgkmcnt(11)
	v_pk_fma_f32 v[190:191], v[74:75], v[232:233], v[190:191]
	ds_read_b128 v[228:231], v118 offset:48128
	v_pk_fma_f32 v[190:191], v[72:73], v[234:235], v[190:191]
	s_waitcnt lgkmcnt(11)
	v_pk_fma_f32 v[190:191], v[70:71], v[240:241], v[190:191]
	ds_read_b128 v[232:235], v118 offset:49152
	v_pk_fma_f32 v[190:191], v[68:69], v[242:243], v[190:191]
	s_waitcnt lgkmcnt(11)
	v_pk_fma_f32 v[190:191], v[66:67], v[244:245], v[190:191]
	ds_read_b128 v[240:243], v118 offset:50176
	v_pk_fma_f32 v[190:191], v[64:65], v[246:247], v[190:191]
	s_waitcnt lgkmcnt(11)
	v_pk_fma_f32 v[190:191], v[62:63], v[248:249], v[190:191]
	ds_read_b128 v[244:247], v118 offset:51200
	v_pk_fma_f32 v[190:191], v[60:61], v[250:251], v[190:191]
	s_waitcnt lgkmcnt(11)
	v_pk_fma_f32 v[190:191], v[58:59], v[196:197], v[190:191]
	ds_read_b128 v[248:251], v118 offset:52224
	v_pk_fma_f32 v[190:191], v[56:57], v[198:199], v[190:191]
	v_add_f32_e32 v2, v190, v191
	v_mov_b32_e32 v88, 0
	s_nop 0
	v_add_f32_dpp v2, v2, v2 row_shr:1 row_mask:0xf bank_mask:0xf bound_ctrl:1
	s_nop 1
	v_add_f32_dpp v2, v2, v2 row_shr:2 row_mask:0xf bank_mask:0xf bound_ctrl:1
	s_nop 1
	v_add_f32_dpp v2, v2, v2 row_shr:4 row_mask:0xf bank_mask:0xf bound_ctrl:1
	s_nop 1
	v_add_f32_dpp v2, v2, v2 row_shr:8 row_mask:0xf bank_mask:0xf bound_ctrl:1
	s_nop 1
	v_mov_b32_dpp v88, v2 row_bcast:15 row_mask:0xa bank_mask:0xf
	v_add_f32_e32 v2, v2, v88
	v_mov_b32_e32 v88, 0
	s_nop 1
	v_mov_b32_dpp v88, v2 row_bcast:31 row_mask:0xc bank_mask:0xf
	v_add_f32_e32 v2, v2, v88
	s_nop 0
	v_readlane_b32 s78, v2, 63
	s_nop 0
	s_waitcnt lgkmcnt(11)
	v_pk_mul_f32 v[192:193], v[86:87], v[200:201]
	ds_read_b128 v[196:199], v118 offset:53248
	v_pk_fma_f32 v[192:193], v[84:85], v[202:203], v[192:193]
	s_waitcnt lgkmcnt(11)
	v_pk_fma_f32 v[192:193], v[82:83], v[204:205], v[192:193]
	ds_read_b128 v[200:203], v118 offset:54272
	v_pk_fma_f32 v[192:193], v[80:81], v[206:207], v[192:193]
	s_waitcnt lgkmcnt(11)
	v_pk_fma_f32 v[192:193], v[78:79], v[208:209], v[192:193]
	ds_read_b128 v[204:207], v118 offset:55296
	v_pk_fma_f32 v[192:193], v[76:77], v[210:211], v[192:193]
	s_waitcnt lgkmcnt(11)
; #define LAS __attribute__((address_space(3)))
; __device__ __forceinline__ float wave_sum(float v) { return lane63(scan64<false>(v)); }
; template <int YMODE, int EXTRA, bool NORM_OUT, bool XN8  , bool XIN_BF = false  , bool XOUT_BF = false  > ...
;     ...
;                     float d8[8];
; #pragma unroll
;                     for (int e = 0; e < 8; ++e) { float s = 0.f;
; #pragma unroll
;                         for (int j = 0; j < 8; ++j) { const f32x4 w = *(const LAS f32x4*)(we + e * D + 256 * j + 4 * F.lane); s += (x[j][0] * w[0] + x[j][1] * w[1]) + (x[j][2] * w[2] + x[j][3] * w[3]); }
;                         d8[e] = wave_sum(s); asm volatile("" ::: "memory"); }
	v_pk_fma_f32 v[192:193], v[74:75], v[212:213], v[192:193]
	ds_read_b128 v[208:211], v118 offset:56320
	v_pk_fma_f32 v[192:193], v[72:73], v[214:215], v[192:193]
	s_waitcnt lgkmcnt(11)
	v_pk_fma_f32 v[192:193], v[70:71], v[216:217], v[192:193]
	ds_read_b128 v[212:215], v118 offset:57344
	v_pk_fma_f32 v[192:193], v[68:69], v[218:219], v[192:193]
	s_waitcnt lgkmcnt(11)
	v_pk_fma_f32 v[192:193], v[66:67], v[220:221], v[192:193]
	ds_read_b128 v[216:219], v118 offset:58368
	v_pk_fma_f32 v[192:193], v[64:65], v[222:223], v[192:193]
	s_waitcnt lgkmcnt(11)
	v_pk_fma_f32 v[192:193], v[62:63], v[224:225], v[192:193]
	ds_read_b128 v[220:223], v118 offset:59392
	v_pk_fma_f32 v[192:193], v[60:61], v[226:227], v[192:193]
	s_waitcnt lgkmcnt(11)
	v_pk_fma_f32 v[192:193], v[58:59], v[228:229], v[192:193]
	ds_read_b128 v[224:227], v118 offset:60416
	v_pk_fma_f32 v[192:193], v[56:57], v[230:231], v[192:193]
	v_add_f32_e32 v2, v192, v193
	v_mov_b32_e32 v88, 0
	s_nop 0
	v_add_f32_dpp v2, v2, v2 row_shr:1 row_mask:0xf bank_mask:0xf bound_ctrl:1
	s_nop 1
	v_add_f32_dpp v2, v2, v2 row_shr:2 row_mask:0xf bank_mask:0xf bound_ctrl:1
	s_nop 1
	v_add_f32_dpp v2, v2, v2 row_shr:4 row_mask:0xf bank_mask:0xf bound_ctrl:1
	s_nop 1
	v_add_f32_dpp v2, v2, v2 row_shr:8 row_mask:0xf bank_mask:0xf bound_ctrl:1
	s_nop 1
	v_mov_b32_dpp v88, v2 row_bcast:15 row_mask:0xa bank_mask:0xf
	v_add_f32_e32 v2, v2, v88
	v_mov_b32_e32 v88, 0
	s_nop 1
	v_mov_b32_dpp v88, v2 row_bcast:31 row_mask:0xc bank_mask:0xf
	v_add_f32_e32 v2, v2, v88
	s_nop 0
	v_readlane_b32 s79, v2, 63
	s_nop 0
	s_waitcnt lgkmcnt(11)
	v_pk_mul_f32 v[190:191], v[86:87], v[232:233]
	ds_read_b128 v[228:231], v118 offset:61440
	v_pk_fma_f32 v[190:191], v[84:85], v[234:235], v[190:191]
	s_waitcnt lgkmcnt(11)
	v_pk_fma_f32 v[190:191], v[82:83], v[240:241], v[190:191]
	ds_read_b128 v[232:235], v118 offset:62464
	v_pk_fma_f32 v[190:191], v[80:81], v[242:243], v[190:191]
	s_waitcnt lgkmcnt(11)
	v_pk_fma_f32 v[190:191], v[78:79], v[244:245], v[190:191]
	ds_read_b128 v[240:243], v118 offset:63488
	v_pk_fma_f32 v[190:191], v[76:77], v[246:247], v[190:191]
	s_waitcnt lgkmcnt(11)
	v_pk_fma_f32 v[190:191], v[74:75], v[248:249], v[190:191]
	ds_read_b128 v[244:247], v118 offset:64512
	v_pk_fma_f32 v[190:191], v[72:73], v[250:251], v[190:191]
	s_waitcnt lgkmcnt(11)
	v_pk_fma_f32 v[190:191], v[70:71], v[196:197], v[190:191]
	v_pk_fma_f32 v[190:191], v[68:69], v[198:199], v[190:191]
	s_waitcnt lgkmcnt(10)
	v_pk_fma_f32 v[190:191], v[66:67], v[200:201], v[190:191]
	v_pk_fma_f32 v[190:191], v[64:65], v[202:203], v[190:191]
	s_waitcnt lgkmcnt(9)
	v_pk_fma_f32 v[190:191], v[62:63], v[204:205], v[190:191]
	v_pk_fma_f32 v[190:191], v[60:61], v[206:207], v[190:191]
	s_waitcnt lgkmcnt(8)
	v_pk_fma_f32 v[190:191], v[58:59], v[208:209], v[190:191]
	v_pk_fma_f32 v[190:191], v[56:57], v[210:211], v[190:191]
	v_add_f32_e32 v2, v190, v191
	v_mov_b32_e32 v88, 0
	s_nop 0
	v_add_f32_dpp v2, v2, v2 row_shr:1 row_mask:0xf bank_mask:0xf bound_ctrl:1
	s_nop 1
	v_add_f32_dpp v2, v2, v2 row_shr:2 row_mask:0xf bank_mask:0xf bound_ctrl:1
	s_nop 1
	v_add_f32_dpp v2, v2, v2 row_shr:4 row_mask:0xf bank_mask:0xf bound_ctrl:1
	s_nop 1
	v_add_f32_dpp v2, v2, v2 row_shr:8 row_mask:0xf bank_mask:0xf bound_ctrl:1
	s_nop 1
	v_mov_b32_dpp v88, v2 row_bcast:15 row_mask:0xa bank_mask:0xf
	v_add_f32_e32 v2, v2, v88
	v_mov_b32_e32 v88, 0
	s_nop 1
	v_mov_b32_dpp v88, v2 row_bcast:31 row_mask:0xc bank_mask:0xf
	v_add_f32_e32 v2, v2, v88
	s_nop 0
	v_readlane_b32 s81, v2, 63
	s_nop 0
	s_waitcnt lgkmcnt(7)
	v_pk_mul_f32 v[192:193], v[86:87], v[212:213]
	v_pk_fma_f32 v[192:193], v[84:85], v[214:215], v[192:193]
	s_waitcnt lgkmcnt(6)
	v_pk_fma_f32 v[192:193], v[82:83], v[216:217], v[192:193]
	v_pk_fma_f32 v[192:193], v[80:81], v[218:219], v[192:193]
	s_waitcnt lgkmcnt(5)
	v_pk_fma_f32 v[192:193], v[78:79], v[220:221], v[192:193]
	v_pk_fma_f32 v[192:193], v[76:77], v[222:223], v[192:193]
	s_waitcnt lgkmcnt(4)
	v_pk_fma_f32 v[192:193], v[74:75], v[224:225], v[192:193]
	v_pk_fma_f32 v[192:193], v[72:73], v[226:227], v[192:193]
	s_waitcnt lgkmcnt(3)
	v_pk_fma_f32 v[192:193], v[70:71], v[228:229], v[192:193]
	v_pk_fma_f32 v[192:193], v[68:69], v[230:231], v[192:193]
	s_waitcnt lgkmcnt(2)
	v_pk_fma_f32 v[192:193], v[66:67], v[232:233], v[192:193]
	v_pk_fma_f32 v[192:193], v[64:65], v[234:235], v[192:193]
	s_waitcnt lgkmcnt(1)
	v_pk_fma_f32 v[192:193], v[62:63], v[240:241], v[192:193]
	v_pk_fma_f32 v[192:193], v[60:61], v[242:243], v[192:193]
	s_waitcnt lgkmcnt(0)
	v_pk_fma_f32 v[192:193], v[58:59], v[244:245], v[192:193]
	v_pk_fma_f32 v[192:193], v[56:57], v[246:247], v[192:193]
	v_add_f32_e32 v2, v192, v193
	v_mov_b32_e32 v56, 0
	s_nop 0
	v_add_f32_dpp v2, v2, v2 row_shr:1 row_mask:0xf bank_mask:0xf bound_ctrl:1
	s_nop 1
	v_add_f32_dpp v2, v2, v2 row_shr:2 row_mask:0xf bank_mask:0xf bound_ctrl:1
	s_nop 1
	v_add_f32_dpp v2, v2, v2 row_shr:4 row_mask:0xf bank_mask:0xf bound_ctrl:1
	s_nop 1
	v_add_f32_dpp v2, v2, v2 row_shr:8 row_mask:0xf bank_mask:0xf bound_ctrl:1
	s_nop 1
	v_mov_b32_dpp v56, v2 row_bcast:15 row_mask:0xa bank_mask:0xf
	v_add_f32_e32 v2, v2, v56
	v_mov_b32_e32 v56, 0
	s_nop 1
	v_mov_b32_dpp v56, v2 row_bcast:31 row_mask:0xc bank_mask:0xf
	v_add_f32_e32 v2, v2, v56
	s_nop 0
	v_readlane_b32 s82, v2, 63
	s_and_saveexec_b64 s[0:1], s[6:7]
	s_cbranch_execz .LBB0_2176
; template <int YMODE, int EXTRA, bool NORM_OUT, bool XN8  , bool XIN_BF = false  , bool XOUT_BF = false  > ...
;     ...
;                         int e1 = 0; float v1 = d8[0];
; #pragma unroll
;                         for (int e = 1; e < 8; ++e) if (d8[e] > v1) { v1 = d8[e]; e1 = e; }
;                         int e2 = -1; float v2 = -3.0e38f;
; #pragma unroll
;                         for (int e = 0; e < 8; ++e) if (e != e1 && d8[e] > v2) { v2 = d8[e]; e2 = e; }
;                         const float w1 = 1.f / (1.f + expf(v2 - v1));
;                         if (F.lane == 0) { routei[rl * 4 + 0] = e1; routei[rl * 4 + 1] = e2; route[rl * 4 + 2] = w1; route[rl * 4 + 3] = 1.f - w1; }
	v_mov_b32_e32 v2, s24
	v_cmp_gt_f32_e64 s[12:13], s25, v2
	v_mov_b32_e32 v56, s25
	v_mov_b32_e32 v58, s26
	v_cndmask_b32_e64 v57, v2, v56, s[12:13]
	v_cmp_gt_f32_e64 s[14:15], s26, v57
	v_mov_b32_e32 v59, s27
	v_mov_b32_e32 v60, s78
	v_cndmask_b32_e64 v57, v57, v58, s[14:15]
	v_cmp_gt_f32_e64 s[16:17], s27, v57
	v_mov_b32_e32 v61, s79
	v_mov_b32_e32 v62, s81
	v_cndmask_b32_e64 v57, v57, v59, s[16:17]
	v_cmp_gt_f32_e64 s[18:19], s78, v57
	v_cndmask_b32_e64 v63, 0, 1, s[12:13]
	s_nop 0
	v_cndmask_b32_e64 v57, v57, v60, s[18:19]
	v_cmp_gt_f32_e64 s[20:21], s79, v57
	s_nop 1
	v_cndmask_b32_e64 v57, v57, v61, s[20:21]
	v_cmp_gt_f32_e64 s[22:23], s81, v57
	s_nop 1
	v_cndmask_b32_e64 v57, v57, v62, s[22:23]
	v_cmp_ngt_f32_e32 vcc, s82, v57
	s_and_b64 s[84:85], s[22:23], vcc
	s_and_b64 s[12:13], s[14:15], exec
	v_readfirstlane_b32 s12, v63
	s_cselect_b32 s14, 2, s12
	s_and_b64 s[12:13], s[16:17], exec
	s_cselect_b32 s14, 3, s14
	s_and_b64 s[12:13], s[18:19], exec
	s_cselect_b32 s14, 4, s14
	s_and_b64 s[12:13], s[20:21], exec
	s_cselect_b32 s14, 5, s14
	s_and_b64 s[12:13], s[22:23], exec
	s_cselect_b32 s14, 6, s14
	s_and_b64 s[12:13], vcc, exec
	s_cselect_b32 s80, s14, 7
	s_cmp_lg_u32 s80, 5
	s_cselect_b64 s[86:87], -1, 0
	s_cmp_lg_u32 s80, 4
	s_cselect_b64 s[22:23], -1, 0
	s_cmp_lg_u32 s80, 3
	s_cselect_b64 s[20:21], -1, 0
	s_cmp_lg_u32 s80, 2
	s_cselect_b64 s[18:19], -1, 0
	s_cmp_lg_u32 s80, 1
	s_cselect_b64 s[16:17], -1, 0
	s_cmp_eq_u32 s80, 0
	s_cselect_b64 s[14:15], -1, 0
	v_cmp_ngt_f32_e64 s[12:13], s24, v126
	s_or_b64 s[12:13], s[12:13], s[14:15]
	s_nop 0
	v_cndmask_b32_e64 v2, v2, v126, s[12:13]
	v_cmp_gt_f32_e64 s[14:15], s25, v2
	s_and_b64 s[14:15], s[16:17], s[14:15]
	s_nop 0
	v_cndmask_b32_e64 v2, v2, v56, s[14:15]
	v_cmp_gt_f32_e64 s[16:17], s26, v2
	s_and_b64 s[16:17], s[18:19], s[16:17]
	v_mov_b32_e32 v56, s82
	v_cndmask_b32_e64 v2, v2, v58, s[16:17]
	v_cmp_gt_f32_e64 s[18:19], s27, v2
	s_and_b64 s[18:19], s[20:21], s[18:19]
	v_cndmask_b32_e64 v58, 0, -1, s[12:13]
	v_cndmask_b32_e64 v2, v2, v59, s[18:19]
	v_cmp_gt_f32_e64 s[20:21], s78, v2
	s_and_b64 s[20:21], s[22:23], s[20:21]
	s_nop 0
	v_cndmask_b32_e64 v2, v2, v60, s[20:21]
	v_cmp_gt_f32_e64 s[22:23], s79, v2
	s_and_b64 s[22:23], s[86:87], s[22:23]
	s_nop 0
	v_cndmask_b32_e64 v2, v2, v61, s[22:23]
	v_cmp_ngt_f32_e64 s[24:25], s81, v2
	s_or_b64 s[24:25], s[84:85], s[24:25]
	s_nop 0
	v_cndmask_b32_e64 v2, v62, v2, s[24:25]
	v_cmp_gt_f32_e64 s[26:27], s82, v2
	s_and_b64 s[26:27], vcc, s[26:27]
	s_and_b64 s[12:13], s[14:15], exec
	v_readfirstlane_b32 s12, v58
	s_cselect_b32 s14, 1, s12
	s_and_b64 s[12:13], s[16:17], exec
	s_cselect_b32 s14, 2, s14
	s_and_b64 s[12:13], s[18:19], exec
	s_cselect_b32 s14, 3, s14
	s_and_b64 s[12:13], s[20:21], exec
	s_cselect_b32 s14, 4, s14
	s_and_b64 s[12:13], s[22:23], exec
	v_cndmask_b32_e64 v2, v2, v56, s[26:27]
	s_cselect_b32 s14, 5, s14
	s_and_b64 s[12:13], s[24:25], exec
	v_cndmask_b32_e32 v56, v56, v57, vcc
	s_cselect_b32 s14, s14, 6
	s_and_b64 s[12:13], s[26:27], exec
	v_sub_f32_e32 v2, v2, v56
	v_mul_f32_e32 v56, 0x3fb8aa3b, v2
	s_mov_b32 s13, 0x3fb8aa3b
	v_fma_f32 v57, v2, s13, -v56
	v_rndne_f32_e32 v58, v56
	v_fmac_f32_e32 v57, 0x32a5705f, v2
	v_sub_f32_e32 v56, v56, v58
	v_add_f32_e32 v56, v56, v57
	v_exp_f32_e32 v56, v56
	v_cvt_i32_f32_e32 v57, v58
	s_mov_b32 s13, 0xc2ce8ed0
	v_cmp_ngt_f32_e32 vcc, s13, v2
	s_mov_b32 s13, 0x42b17218
	v_ldexp_f32 v56, v56, v57
	v_cndmask_b32_e32 v56, 0, v56, vcc
	v_cmp_nlt_f32_e32 vcc, s13, v2
	s_cselect_b32 s12, 7, s14
	s_lshl_b32 s13, s42, 4
	v_cndmask_b32_e32 v2, v127, v56, vcc
	v_add_f32_e32 v2, 1.0, v2
	v_div_scale_f32 v56, s[14:15], v2, v2, 1.0
	v_rcp_f32_e32 v57, v56
	s_add_i32 s13, s13, 0
	s_add_i32 s13, s13, 0x16000
	v_fma_f32 v58, -v56, v57, 1.0
	v_fmac_f32_e32 v57, v58, v57
	v_div_scale_f32 v58, vcc, 1.0, v2, 1.0
	v_mul_f32_e32 v59, v58, v57
	v_fma_f32 v60, -v56, v59, v58
	v_fmac_f32_e32 v59, v60, v57
	v_fma_f32 v56, -v56, v59, v58
	v_div_fmas_f32 v56, v56, v57, v59
	v_div_fixup_f32 v58, v56, v2, 1.0
	v_sub_f32_e32 v59, 1.0, v58
	v_mov_b32_e32 v56, s80
	v_mov_b32_e32 v57, s12
	v_mov_b32_e32 v2, s13
	ds_write_b128 v2, v[56:59]
	s_branch .LBB0_2176
